# nt hint on single-use cold input reads: x rows in prologue HN and layer-0 post-mix, ada_w in the modulation GEMV
# baseline (speedup 1.0000x reference)
; #define GAS __attribute__((address_space(1)))
; #define LAS __attribute__((address_space(3)))
; __device__ __forceinline__ void mod_item(Frame& F, int it) {
;     ...
;     const int cl = tid & 15, kq = tid >> 4;
;     const GAS float* W = INP(F, I_ADAW) + (size_t)l * DM * 6144 + cg * 64 + cl * 4;
;     f32x4 acc[4];
; #pragma unroll
;     for (int b = 0; b < 4; ++b) acc[b] = (f32x4){0.f, 0.f, 0.f, 0.f};
; #pragma unroll 4
;     for (int kk = 0; kk < 32; ++kk) { const int k = kq * 32 + kk; const f32x4 w = *(const GAS f32x4*)(W + (size_t)k * 6144);
; #pragma unroll
;         for (int b = 0; b < 4; ++b) acc[b] += w * cond[b * DM + k]; }
; #pragma unroll
;     for (int b = 0; b < 4; ++b) *(LAS f32x4*)(part + (kq * 4 + b) * 64 + cl * 4) = acc[b];
;     __syncthreads();
;     if (tid < 256) { const int b = tid >> 6, col = tid & 63; float s = 0.f;
;         for (int q = 0; q < 32; ++q) s += part[(q * 4 + b) * 64 + col];
;         GAS float* mod = (GAS float*)(F.ws + WS_MOD);
;         mod[(size_t)(l * 4 + b) * 6144 + cg * 64 + col] = s + INP(F, I_ADAB)[l * 6144 + cg * 64 + col]; }
;     __syncthreads();
.LBB0_21:
	v_lshl_add_u64 v[38:39], v[24:25], 0, s[12:13]
	v_add_co_u32_e32 v50, vcc, s16, v38
	global_load_dwordx4 v[34:37], v[38:39], off nt
	s_nop 0
	v_addc_co_u32_e32 v51, vcc, 0, v39, vcc
	v_add_co_u32_e32 v52, vcc, s18, v38
	s_add_u32 s12, s12, 0x18000
	s_nop 0
	v_addc_co_u32_e32 v53, vcc, 0, v39, vcc
	v_add_co_u32_e32 v54, vcc, s19, v38
	s_addc_u32 s13, s13, 0
	s_nop 0
	v_addc_co_u32_e32 v55, vcc, 0, v39, vcc
	global_load_dwordx4 v[38:41], v[50:51], off nt
	global_load_dwordx4 v[42:45], v[52:53], off nt
	global_load_dwordx4 v[46:49], v[54:55], off nt
	ds_read_b128 v[50:53], v33
	ds_read_b128 v[54:57], v33 offset:4096
	ds_read_b128 v[58:61], v33 offset:8192
	ds_read_b128 v[62:65], v33 offset:12288
	v_add_u32_e32 v33, 16, v33
	s_waitcnt lgkmcnt(3)
	v_mov_b32_e32 v66, v53
	s_waitcnt lgkmcnt(2)
	v_mov_b32_e32 v68, v57
	s_waitcnt lgkmcnt(1)
	v_mov_b32_e32 v70, v61
	s_waitcnt lgkmcnt(0)
	v_mov_b32_e32 v72, v65
	s_cmp_eq_u32 s12, 0xc0000
	s_waitcnt vmcnt(3)
	v_pk_fma_f32 v[8:9], v[36:37], v[50:51], v[8:9] op_sel_hi:[1,0,1]
	v_pk_fma_f32 v[6:7], v[34:35], v[50:51], v[6:7] op_sel_hi:[1,0,1]
	v_pk_fma_f32 v[12:13], v[36:37], v[54:55], v[12:13] op_sel_hi:[1,0,1]
	v_pk_fma_f32 v[10:11], v[34:35], v[54:55], v[10:11] op_sel_hi:[1,0,1]
	v_pk_fma_f32 v[16:17], v[36:37], v[58:59], v[16:17] op_sel_hi:[1,0,1]
	v_pk_fma_f32 v[14:15], v[34:35], v[58:59], v[14:15] op_sel_hi:[1,0,1]
	v_pk_fma_f32 v[4:5], v[36:37], v[62:63], v[4:5] op_sel_hi:[1,0,1]
	v_pk_fma_f32 v[2:3], v[34:35], v[62:63], v[2:3] op_sel_hi:[1,0,1]
	s_waitcnt vmcnt(2)
	v_pk_fma_f32 v[6:7], v[38:39], v[50:51], v[6:7] op_sel:[0,1,0]
	v_pk_fma_f32 v[8:9], v[40:41], v[50:51], v[8:9] op_sel:[0,1,0]
	v_pk_fma_f32 v[10:11], v[38:39], v[54:55], v[10:11] op_sel:[0,1,0]
	v_pk_fma_f32 v[12:13], v[40:41], v[54:55], v[12:13] op_sel:[0,1,0]
	v_pk_fma_f32 v[14:15], v[38:39], v[58:59], v[14:15] op_sel:[0,1,0]
	v_pk_fma_f32 v[16:17], v[40:41], v[58:59], v[16:17] op_sel:[0,1,0]
	v_pk_fma_f32 v[2:3], v[38:39], v[62:63], v[2:3] op_sel:[0,1,0]
	v_pk_fma_f32 v[4:5], v[40:41], v[62:63], v[4:5] op_sel:[0,1,0]
	s_waitcnt vmcnt(1)
	v_pk_fma_f32 v[8:9], v[44:45], v[52:53], v[8:9] op_sel_hi:[1,0,1]
	v_pk_fma_f32 v[6:7], v[42:43], v[52:53], v[6:7] op_sel_hi:[1,0,1]
	v_pk_fma_f32 v[12:13], v[44:45], v[56:57], v[12:13] op_sel_hi:[1,0,1]
	v_pk_fma_f32 v[10:11], v[42:43], v[56:57], v[10:11] op_sel_hi:[1,0,1]
	v_pk_fma_f32 v[16:17], v[44:45], v[60:61], v[16:17] op_sel_hi:[1,0,1]
	v_pk_fma_f32 v[14:15], v[42:43], v[60:61], v[14:15] op_sel_hi:[1,0,1]
	v_pk_fma_f32 v[4:5], v[44:45], v[64:65], v[4:5] op_sel_hi:[1,0,1]
	v_pk_fma_f32 v[2:3], v[42:43], v[64:65], v[2:3] op_sel_hi:[1,0,1]
	s_waitcnt vmcnt(0)
	v_pk_fma_f32 v[8:9], v[48:49], v[66:67], v[8:9] op_sel_hi:[1,0,1]
	v_pk_fma_f32 v[6:7], v[46:47], v[66:67], v[6:7] op_sel_hi:[1,0,1]
	v_pk_fma_f32 v[12:13], v[48:49], v[68:69], v[12:13] op_sel_hi:[1,0,1]
	v_pk_fma_f32 v[10:11], v[46:47], v[68:69], v[10:11] op_sel_hi:[1,0,1]
	v_pk_fma_f32 v[16:17], v[48:49], v[70:71], v[16:17] op_sel_hi:[1,0,1]
	v_pk_fma_f32 v[14:15], v[46:47], v[70:71], v[14:15] op_sel_hi:[1,0,1]
	v_pk_fma_f32 v[4:5], v[48:49], v[72:73], v[4:5] op_sel_hi:[1,0,1]
	v_pk_fma_f32 v[2:3], v[46:47], v[72:73], v[2:3] op_sel_hi:[1,0,1]
	s_cbranch_scc0 .LBB0_21
	ds_write_b128 v1, v[6:9] offset:16384
	ds_write_b128 v1, v[10:13] offset:16640
	ds_write_b128 v1, v[14:17] offset:16896
	ds_write_b128 v1, v[2:5] offset:17152
	s_waitcnt lgkmcnt(0)
	s_barrier
	s_and_saveexec_b64 s[12:13], s[4:5]
	s_cbranch_execz .LBB0_16
	v_mov_b32_e32 v2, s20
	ds_read_b64 v[2:3], v2
	s_mul_i32 s23, s22, 0x1800
	s_add_i32 s23, s23, s10
	v_or_b32_e32 v4, s23, v186
	v_ashrrev_i32_e32 v5, 31, v4
	s_waitcnt lgkmcnt(0)
	v_readfirstlane_b32 s24, v2
	v_readfirstlane_b32 s25, v3
	v_lshl_add_u32 v50, s22, 2, v27
	v_mov_b32_e32 v2, s24
	v_mov_b32_e32 v3, s25
	v_lshl_add_u64 v[2:3], v[4:5], 2, v[2:3]
	global_load_dword v33, v[2:3], off
	ds_read2st64_b32 v[2:3], v26 offset0:64 offset1:68
	ds_read2st64_b32 v[4:5], v26 offset0:72 offset1:76
	ds_read2st64_b32 v[6:7], v26 offset0:80 offset1:84
	ds_read2st64_b32 v[8:9], v26 offset0:88 offset1:92
	ds_read2st64_b32 v[10:11], v26 offset0:96 offset1:100
	ds_read2st64_b32 v[12:13], v26 offset0:104 offset1:108
	ds_read2st64_b32 v[14:15], v26 offset0:112 offset1:116
	ds_read2st64_b32 v[16:17], v26 offset0:120 offset1:124
	ds_read2st64_b32 v[24:25], v26 offset0:128 offset1:132
	ds_read2st64_b32 v[34:35], v26 offset0:136 offset1:140
	ds_read2st64_b32 v[36:37], v26 offset0:144 offset1:148
	ds_read2st64_b32 v[38:39], v26 offset0:152 offset1:156
	ds_read2st64_b32 v[40:41], v26 offset0:160 offset1:164
	ds_read2st64_b32 v[42:43], v26 offset0:168 offset1:172
	ds_read2st64_b32 v[44:45], v26 offset0:176 offset1:180
	ds_read2st64_b32 v[46:47], v26 offset0:184 offset1:188
	s_waitcnt lgkmcnt(14)
	v_add_f32_e32 v2, 0, v2
	v_add_f32_e32 v2, v2, v3
	v_add_f32_e32 v2, v2, v4
	v_add_f32_e32 v2, v2, v5
	s_waitcnt lgkmcnt(13)
	v_add_f32_e32 v2, v2, v6
	v_add_f32_e32 v2, v2, v7
	s_waitcnt lgkmcnt(12)
	v_add_f32_e32 v2, v2, v8
	v_add_f32_e32 v2, v2, v9
	s_waitcnt lgkmcnt(11)
	v_add_f32_e32 v2, v2, v10
	v_add_f32_e32 v2, v2, v11
	s_waitcnt lgkmcnt(10)
	v_add_f32_e32 v2, v2, v12
	v_add_f32_e32 v2, v2, v13
	s_waitcnt lgkmcnt(9)
	v_add_f32_e32 v2, v2, v14
	v_add_f32_e32 v2, v2, v15
	s_waitcnt lgkmcnt(8)
	v_add_f32_e32 v2, v2, v16
	v_add_f32_e32 v2, v2, v17
	s_waitcnt lgkmcnt(7)
	v_add_f32_e32 v2, v2, v24
	v_add_f32_e32 v2, v2, v25
	s_waitcnt lgkmcnt(6)
	v_add_f32_e32 v2, v2, v34
	v_add_f32_e32 v2, v2, v35
	s_waitcnt lgkmcnt(5)
	v_add_f32_e32 v2, v2, v36
	v_add_f32_e32 v2, v2, v37
	s_waitcnt lgkmcnt(4)
	v_add_f32_e32 v2, v2, v38
	v_add_f32_e32 v2, v2, v39
	s_waitcnt lgkmcnt(3)
	v_add_f32_e32 v2, v2, v40
	v_add_f32_e32 v2, v2, v41
	s_waitcnt lgkmcnt(2)
	v_add_f32_e32 v2, v2, v42
	v_add_f32_e32 v2, v2, v43
	s_waitcnt lgkmcnt(1)
	v_add_f32_e32 v2, v2, v44
	v_mov_b64_e32 v[48:49], s[2:3]
	v_add_f32_e32 v2, v2, v45
	v_mad_i64_i32 v[48:49], s[22:23], v50, s16, v[48:49]
	s_waitcnt lgkmcnt(0)
	v_add_f32_e32 v2, v2, v46
	v_lshl_add_u64 v[48:49], s[10:11], 2, v[48:49]
	v_add_f32_e32 v2, v2, v47
	s_waitcnt vmcnt(0)
	v_add_f32_e32 v4, v2, v33
	v_lshl_add_u64 v[2:3], v[48:49], 0, v[18:19]
	global_store_dword v[2:3], v4, off
	s_branch .LBB0_16

; #define GAS __attribute__((address_space(1)))
; #define LAS __attribute__((address_space(3)))
; __device__ __forceinline__ unsigned pk2(float lo, float hi) { const m_f32x2 v = {lo, hi}; return __builtin_bit_cast(unsigned, __builtin_convertvector(v, m_bf16x2)); }
; __device__ __forceinline__ float rsq(float x) { return __builtin_amdgcn_rsqf(x); }
; __device__ __forceinline__ void prologue2(Frame& F) {
;     ...
;     for (int m = gw; m < M; m += NGW) { const int b = m >> 12; f32x4 v[4]; row_load(INP(F, I_X) + (size_t)m * DM, lane, v);
;         const LAS f32x4* Bv = (const LAS f32x4*)(PV + b * 2048); const float rstd = rsq(row_ss(v, lane) * (1.0f / DM) + EPS); GAS v2u* orow = (GAS v2u*)((GAS bf16*)(F.ws + WS_HN) + (size_t)m * DM);
; #pragma unroll
;         for (int j = 0; j < 4; ++j) { const int c4 = lane + 64 * j; const f32x4 o4 = v[j] * rstd * Bv[c4] + Bv[256 + c4]; v2u o; o.x = pk2(o4[0], o4[1]); o.y = pk2(o4[2], o4[3]); orow[c4] = o; } }
.LBB0_132:
	s_waitcnt lgkmcnt(0)
	v_readfirstlane_b32 s8, v2
	v_readfirstlane_b32 s9, v3
	s_lshl_b32 s5, s1, 1
	s_and_b32 s5, s5, 0xffffe000
	v_lshl_add_u64 v[26:27], s[8:9], 0, v[8:9]
	global_load_dwordx4 v[10:13], v[26:27], off nt
	global_load_dwordx4 v[14:17], v[26:27], off offset:1024 nt
	global_load_dwordx4 v[18:21], v[26:27], off offset:2048 nt
	global_load_dwordx4 v[22:25], v[26:27], off offset:3072 nt
	v_add_u32_e32 v54, s5, v1
	ds_read_b128 v[26:29], v54
	ds_read_b128 v[30:33], v54 offset:1024
	ds_read_b128 v[34:37], v54 offset:4096
	ds_read_b128 v[38:41], v54 offset:5120
	ds_read_b128 v[42:45], v54 offset:2048
	ds_read_b128 v[46:49], v54 offset:3072
	ds_read_b128 v[50:53], v54 offset:6144
	ds_read_b128 v[54:57], v54 offset:7168
	s_add_i32 s1, s1, s4
	v_lshl_add_u64 v[8:9], v[8:9], 0, s[6:7]
	s_cmpk_lt_i32 s1, 0x4000
	s_waitcnt vmcnt(0)
	v_mul_f32_e32 v58, v11, v11
	v_mul_f32_e32 v59, v13, v13
	v_mul_f32_e32 v60, v15, v15
	v_mul_f32_e32 v61, v17, v17
	v_mul_f32_e32 v62, v19, v19
	v_mul_f32_e32 v63, v21, v21
	v_fmac_f32_e32 v58, v10, v10
	v_fmac_f32_e32 v59, v12, v12
	v_fmac_f32_e32 v60, v14, v14
	v_fmac_f32_e32 v61, v16, v16
	v_mul_f32_e32 v64, v23, v23
	v_mul_f32_e32 v65, v25, v25
	v_fmac_f32_e32 v62, v18, v18
	v_fmac_f32_e32 v63, v20, v20
	v_add_f32_e32 v58, v58, v59
	v_add_f32_e32 v59, v60, v61
	v_fmac_f32_e32 v64, v22, v22
	v_fmac_f32_e32 v65, v24, v24
	v_add_f32_e32 v60, v62, v63
	v_add_f32_e32 v58, v58, v59
	v_add_f32_e32 v61, v64, v65
	v_add_f32_e32 v58, v58, v60
	v_add_f32_e32 v58, v58, v61
	s_nop 1
	v_add_f32_dpp v58, v58, v58 quad_perm:[1,0,3,2] row_mask:0xf bank_mask:0xf bound_ctrl:1
	s_nop 1
	v_add_f32_dpp v58, v58, v58 quad_perm:[2,3,0,1] row_mask:0xf bank_mask:0xf bound_ctrl:1
	s_nop 1
	v_add_f32_dpp v58, v58, v58 row_half_mirror row_mask:0xf bank_mask:0xf bound_ctrl:1
	s_nop 1
	v_add_f32_dpp v58, v58, v58 row_mirror row_mask:0xf bank_mask:0xf bound_ctrl:1
	v_mov_b32_e32 v59, v58
	s_nop 1
	v_permlane16_swap_b32_e32 v58, v59
	v_add_f32_e32 v58, v58, v59
	v_mov_b32_e32 v59, v58
	s_nop 1
	v_permlane32_swap_b32_e32 v58, v59
	v_add_f32_e32 v58, v58, v59
	v_fmamk_f32 v58, v58, 0x3a800000, v7
	v_rsq_f32_e32 v58, v58
	s_nop 0
	v_pk_mul_f32 v[10:11], v[10:11], v[58:59] op_sel_hi:[1,0]
	v_pk_mul_f32 v[12:13], v[12:13], v[58:59] op_sel_hi:[1,0]
	v_pk_mul_f32 v[14:15], v[14:15], v[58:59] op_sel_hi:[1,0]
	v_pk_mul_f32 v[16:17], v[16:17], v[58:59] op_sel_hi:[1,0]
	v_pk_mul_f32 v[18:19], v[18:19], v[58:59] op_sel_hi:[1,0]
	v_pk_mul_f32 v[20:21], v[20:21], v[58:59] op_sel_hi:[1,0]
	v_pk_mul_f32 v[22:23], v[22:23], v[58:59] op_sel_hi:[1,0]
	v_pk_mul_f32 v[24:25], v[24:25], v[58:59] op_sel_hi:[1,0]
	s_waitcnt lgkmcnt(5)
	v_pk_fma_f32 v[12:13], v[28:29], v[12:13], v[36:37]
	v_pk_fma_f32 v[10:11], v[26:27], v[10:11], v[34:35]
	s_waitcnt lgkmcnt(4)
	v_pk_fma_f32 v[16:17], v[32:33], v[16:17], v[40:41]
	v_pk_fma_f32 v[14:15], v[30:31], v[14:15], v[38:39]
	s_waitcnt lgkmcnt(1)
	v_pk_fma_f32 v[20:21], v[44:45], v[20:21], v[52:53]
	v_pk_fma_f32 v[18:19], v[42:43], v[18:19], v[50:51]
	s_waitcnt lgkmcnt(0)
	v_pk_fma_f32 v[24:25], v[24:25], v[48:49], v[56:57]
	v_pk_fma_f32 v[22:23], v[22:23], v[46:47], v[54:55]
	v_cvt_pk_bf16_f32 v10, v10, v11
	v_cvt_pk_bf16_f32 v11, v12, v13
	v_cvt_pk_bf16_f32 v12, v14, v15
	v_cvt_pk_bf16_f32 v13, v16, v17
	v_cvt_pk_bf16_f32 v14, v18, v19
	v_cvt_pk_bf16_f32 v15, v20, v21
	v_cvt_pk_bf16_f32 v16, v22, v23
	v_cvt_pk_bf16_f32 v17, v24, v25
	global_store_dwordx2 v[4:5], v[10:11], off
	global_store_dwordx2 v[4:5], v[12:13], off offset:512
	global_store_dwordx2 v[4:5], v[14:15], off offset:1024
	global_store_dwordx2 v[4:5], v[16:17], off offset:1536
	v_lshl_add_u64 v[4:5], v[4:5], 0, s[2:3]
	s_cbranch_scc1 .LBB0_132

; #define GAS __attribute__((address_space(1)))
; #define LAS __attribute__((address_space(3)))
; __device__ __forceinline__ float rsq(float x) { return __builtin_amdgcn_rsqf(x); }
; __device__ __forceinline__ void post_mix_front(Frame& F, int l, int m, const f32x4 (&y)[4], f32x4 (&x)[4], const LAS float* PV) {
;     const int lane = F.lane, b = m >> 12; const LAS f32x4* A = (const LAS f32x4*)(PV + b * 3072); const LAS f32x4* Bv = A + 256; const LAS f32x4* Cv = A + 512;
;     const float rstd = rsq(row_ss(y, lane) * (1.0f / DM) + EPS);
; #pragma unroll
;     for (int j = 0; j < 4; ++j) { const int c4 = lane + 64 * j; x[j] = x[j] + A[c4] * (y[j] * rstd); }
;     roww_store_bf16((GAS bf16*)(F.ws + WS_XR) + (size_t)m * DM, lane, x);
;     const float rstd2 = rsq(row_ss(x, lane) * (1.0f / DM) + EPS);
; __device__ __forceinline__ void phase_post_mix(Frame& F, int l) {
;     ...
;     for (int m0 = gw; m0 < M; m0 += 4 * NGW) {
;         int mm[4]; f32x4 xx[4][4];
; #pragma unroll
;         for (int q = 0; q < 4; ++q) mm[q] = (m0 + q * NGW < M) ? m0 + q * NGW : m0;
; #pragma unroll
;         for (int q = 0; q < 4; q += 2) { f32x4 ya[4], yb[4];
;             roww_load_bf16(Y + (size_t)mm[q] * DM, lane, ya); roww_load_bf16(Y + (size_t)mm[q + 1] * DM, lane, yb);
;             if (l == 0) { roww_load(xin + (size_t)mm[q] * DM, lane, xx[q]); roww_load(xin + (size_t)mm[q + 1] * DM, lane, xx[q + 1]); }
;             else { roww_load_bf16(xr + (size_t)mm[q] * DM, lane, xx[q]); roww_load_bf16(xr + (size_t)mm[q + 1] * DM, lane, xx[q + 1]); }
;             post_mix_front(F, l, mm[q], ya, xx[q], PV); post_mix_front(F, l, mm[q + 1], yb, xx[q + 1], PV); }
.LBB0_1249:
	v_lshl_add_u64 v[54:55], s[80:81], 0, v[46:47]
	v_add_co_u32_e32 v2, vcc, 0x10400000, v54
	s_mov_b64 s[2:3], 0x10400000
	s_nop 0
	v_addc_co_u32_e32 v3, vcc, 0, v55, vcc
	global_load_dwordx4 v[10:13], v[2:3], off
	v_lshl_add_u64 v[2:3], v[54:55], 0, s[2:3]
	global_load_dwordx4 v[14:17], v[2:3], off offset:16
	s_add_i32 s2, s42, s14
	s_cmpk_lt_i32 s2, 0x4000
	s_cselect_b32 s28, s2, s14
	s_add_i32 s2, s15, s14
	s_cmpk_lt_i32 s2, 0x4000
	s_cselect_b32 s26, s2, s14
	s_add_i32 s2, s17, s14
	s_cmpk_lt_i32 s2, 0x4000
	s_cselect_b32 s24, s2, s14
	s_ashr_i32 s29, s28, 31
	s_lshl_b64 s[2:3], s[28:29], 11
	v_lshl_add_u64 v[2:3], v[34:35], 0, s[2:3]
	global_load_dwordx4 v[50:53], v[2:3], off
	global_load_dwordx4 v[76:79], v[2:3], off offset:16
	global_load_dwordx4 v[18:21], v[48:49], off offset:16 nt
	global_load_dwordx4 v[22:25], v[48:49], off nt
	global_load_dwordx4 v[26:29], v[48:49], off offset:-16 nt
	global_load_dwordx4 v[30:33], v[48:49], off offset:-32 nt
	s_ashr_i32 s30, s14, 12
	s_lshl_b64 s[34:35], s[28:29], 12
	s_mul_i32 s25, s30, 0x3000
	v_lshl_add_u64 v[80:81], v[36:37], 0, s[34:35]
	v_add_u32_e32 v91, s25, v98
	global_load_dwordx4 v[2:5], v[80:81], off offset:48 nt
	global_load_dwordx4 v[6:9], v[80:81], off offset:32 nt
	s_mov_b32 s25, 0x27400000
	s_ashr_i32 s34, s28, 12
	s_lshl_b64 s[36:37], s[28:29], 10
	s_ashr_i32 s27, s26, 31
	s_lshl_b64 s[38:39], s[26:27], 11
	s_lshl_b64 s[40:41], s[26:27], 10
	s_waitcnt vmcnt(0)
	v_and_b32_e32 v83, 0xffff0000, v10
	v_and_b32_e32 v85, 0xffff0000, v11
	v_and_b32_e32 v87, 0xffff0000, v12
	v_and_b32_e32 v89, 0xffff0000, v13
	v_lshlrev_b32_e32 v82, 16, v10
	v_lshlrev_b32_e32 v84, 16, v11
	v_lshlrev_b32_e32 v86, 16, v12
	v_lshlrev_b32_e32 v88, 16, v13
	v_and_b32_e32 v75, 0xffff0000, v14
	v_and_b32_e32 v73, 0xffff0000, v15
	v_mul_f32_e32 v10, v83, v83
	v_mul_f32_e32 v11, v85, v85
	v_mul_f32_e32 v12, v87, v87
	v_mul_f32_e32 v13, v89, v89
	v_lshlrev_b32_e32 v74, 16, v14
	v_lshlrev_b32_e32 v72, 16, v15
	v_and_b32_e32 v67, 0xffff0000, v16
	v_and_b32_e32 v61, 0xffff0000, v17
	v_mul_f32_e32 v14, v75, v75
	v_mul_f32_e32 v15, v73, v73
	v_fmac_f32_e32 v10, v82, v82
	v_fmac_f32_e32 v11, v84, v84
	v_fmac_f32_e32 v12, v86, v86
	v_fmac_f32_e32 v13, v88, v88
	v_lshlrev_b32_e32 v66, 16, v16
	v_lshlrev_b32_e32 v60, 16, v17
	v_mul_f32_e32 v16, v67, v67
	v_mul_f32_e32 v17, v61, v61
	v_fmac_f32_e32 v14, v74, v74
	v_fmac_f32_e32 v15, v72, v72
	v_add_f32_e32 v10, v10, v11
	v_add_f32_e32 v11, v12, v13
	v_fmac_f32_e32 v16, v66, v66
	v_fmac_f32_e32 v17, v60, v60
	v_add_f32_e32 v12, v14, v15
	v_add_f32_e32 v10, v10, v11
	v_add_f32_e32 v13, v16, v17
	v_add_f32_e32 v10, v10, v12
	v_add_f32_e32 v10, v13, v10
	v_lshlrev_b32_e32 v70, 16, v50
	v_and_b32_e32 v71, 0xffff0000, v50
	v_add_f32_dpp v10, v10, v10 quad_perm:[1,0,3,2] row_mask:0xf bank_mask:0xf bound_ctrl:1
	v_lshlrev_b32_e32 v68, 16, v51
	v_and_b32_e32 v69, 0xffff0000, v51
	v_add_f32_dpp v10, v10, v10 quad_perm:[2,3,0,1] row_mask:0xf bank_mask:0xf bound_ctrl:1
	v_lshlrev_b32_e32 v64, 16, v52
	v_and_b32_e32 v65, 0xffff0000, v52
	v_add_f32_dpp v10, v10, v10 row_half_mirror row_mask:0xf bank_mask:0xf bound_ctrl:1
	v_lshlrev_b32_e32 v62, 16, v53
	v_and_b32_e32 v63, 0xffff0000, v53
	v_add_f32_dpp v10, v10, v10 row_mirror row_mask:0xf bank_mask:0xf bound_ctrl:1
	v_mov_b32_e32 v11, v10
	s_nop 1
	v_permlane16_swap_b32_e32 v10, v11
	v_add_f32_e32 v10, v10, v11
	v_mov_b32_e32 v11, v10
	s_nop 1
	v_permlane32_swap_b32_e32 v10, v11
	v_add_f32_e32 v10, v10, v11
	v_fmamk_f32 v10, v10, 0x3a800000, v225
	v_rsq_f32_e32 v90, v10
	v_lshlrev_b32_e32 v58, 16, v76
	v_and_b32_e32 v59, 0xffff0000, v76
	v_lshlrev_b32_e32 v56, 16, v77
	v_and_b32_e32 v57, 0xffff0000, v77
	v_lshlrev_b32_e32 v52, 16, v78
	v_and_b32_e32 v53, 0xffff0000, v78
	v_lshlrev_b32_e32 v50, 16, v79
	v_and_b32_e32 v51, 0xffff0000, v79
	ds_read_b128 v[76:79], v91
	global_load_dwordx4 v[10:13], v[80:81], off offset:16 nt
	global_load_dwordx4 v[14:17], v[80:81], off nt
	v_pk_mul_f32 v[92:93], v[90:91], v[82:83] op_sel_hi:[0,1]
	ds_read_b128 v[80:83], v91 offset:1024
	v_pk_mul_f32 v[84:85], v[90:91], v[84:85] op_sel_hi:[0,1]
	s_waitcnt lgkmcnt(1)
	v_pk_fma_f32 v[76:77], v[76:77], v[92:93], v[30:31]
	v_pk_mul_f32 v[30:31], v[90:91], v[88:89] op_sel_hi:[0,1]
	v_pk_fma_f32 v[32:33], v[78:79], v[84:85], v[32:33]
	v_pk_mul_f32 v[78:79], v[90:91], v[86:87] op_sel_hi:[0,1]
	s_waitcnt lgkmcnt(0)
	v_pk_fma_f32 v[82:83], v[82:83], v[30:31], v[28:29]
	ds_read_b128 v[28:31], v91 offset:2048
	v_pk_fma_f32 v[78:79], v[80:81], v[78:79], v[26:27]
	v_pk_mul_f32 v[26:27], v[90:91], v[74:75] op_sel_hi:[0,1]
	v_pk_mul_f32 v[80:81], v[90:91], v[72:73] op_sel_hi:[0,1]
	ds_read_b128 v[72:75], v91 offset:3072
	s_waitcnt lgkmcnt(1)
	v_pk_fma_f32 v[80:81], v[30:31], v[80:81], v[24:25]
	v_pk_fma_f32 v[84:85], v[28:29], v[26:27], v[22:23]
	v_pk_mul_f32 v[22:23], v[90:91], v[66:67] op_sel_hi:[0,1]
	v_pk_mul_f32 v[24:25], v[90:91], v[60:61] op_sel_hi:[0,1]
	v_add_co_u32_e32 v26, vcc, s25, v54
	s_waitcnt lgkmcnt(0)
; #define GAS __attribute__((address_space(1)))
; #define LAS __attribute__((address_space(3)))
; __device__ __forceinline__ float rsq(float x) { return __builtin_amdgcn_rsqf(x); }
; __device__ __forceinline__ void post_mix_front(Frame& F, int l, int m, const f32x4 (&y)[4], f32x4 (&x)[4], const LAS float* PV) {
;     const int lane = F.lane, b = m >> 12; const LAS f32x4* A = (const LAS f32x4*)(PV + b * 3072); const LAS f32x4* Bv = A + 256; const LAS f32x4* Cv = A + 512;
;     const float rstd = rsq(row_ss(y, lane) * (1.0f / DM) + EPS);
; #pragma unroll
;     for (int j = 0; j < 4; ++j) { const int c4 = lane + 64 * j; x[j] = x[j] + A[c4] * (y[j] * rstd); }
;     roww_store_bf16((GAS bf16*)(F.ws + WS_XR) + (size_t)m * DM, lane, x);
;     const float rstd2 = rsq(row_ss(x, lane) * (1.0f / DM) + EPS);
;     v4u hw;
; #pragma unroll
;     for (int j = 0; j < 4; ++j) { const int c4 = lane + 64 * j; x[j] = x[j] * rstd2 * Bv[c4] + Cv[c4]; hw[j] = pk4_f8(x[j][0], x[j][1], x[j][2], x[j][3]); }
;     ((GAS v4u*)((GAS unsigned char*)(F.ws + WS_HN) + (size_t)m * DM))[lane] = hw;
; }
	v_pk_fma_f32 v[86:87], v[74:75], v[24:25], v[20:21]
	v_pk_fma_f32 v[88:89], v[72:73], v[22:23], v[18:19]
	v_cvt_pk_bf16_f32 v18, v76, v77
	v_cvt_pk_bf16_f32 v19, v32, v33
	v_cvt_pk_bf16_f32 v20, v78, v79
	v_cvt_pk_bf16_f32 v21, v82, v83
	v_addc_co_u32_e32 v27, vcc, 0, v55, vcc
	global_store_dwordx4 v[26:27], v[18:21], off
	v_cvt_pk_bf16_f32 v22, v84, v85
	v_cvt_pk_bf16_f32 v23, v80, v81
	v_mul_f32_e32 v18, v77, v77
	v_mul_f32_e32 v19, v33, v33
	v_fmac_f32_e32 v18, v76, v76
	v_fmac_f32_e32 v19, v32, v32
	v_add_f32_e32 v18, v18, v19
	v_mul_f32_e32 v19, v79, v79
	v_mul_f32_e32 v20, v83, v83
	v_fmac_f32_e32 v19, v78, v78
	v_fmac_f32_e32 v20, v82, v82
	v_add_f32_e32 v19, v19, v20
	v_add_f32_e32 v18, v18, v19
	v_mul_f32_e32 v19, v85, v85
	v_mul_f32_e32 v20, v81, v81
	v_fmac_f32_e32 v19, v84, v84
	v_fmac_f32_e32 v20, v80, v80
	v_add_f32_e32 v19, v19, v20
	v_add_f32_e32 v18, v19, v18
	v_mul_f32_e32 v19, v89, v89
	v_mul_f32_e32 v20, v87, v87
	v_fmac_f32_e32 v19, v88, v88
	v_fmac_f32_e32 v20, v86, v86
	v_add_f32_e32 v19, v19, v20
	v_add_f32_e32 v18, v19, v18
	v_cvt_pk_bf16_f32 v24, v88, v89
	v_cvt_pk_bf16_f32 v25, v86, v87
	v_add_f32_dpp v18, v18, v18 quad_perm:[1,0,3,2] row_mask:0xf bank_mask:0xf bound_ctrl:1
	global_store_dwordx4 v[26:27], v[22:25], off offset:16
	v_mov_b32_e32 v72, v183
	v_add_f32_dpp v18, v18, v18 quad_perm:[2,3,0,1] row_mask:0xf bank_mask:0xf bound_ctrl:1
	v_mov_b32_e32 v73, v183
	v_mov_b32_e32 v74, v183
	v_add_f32_dpp v18, v18, v18 row_half_mirror row_mask:0xf bank_mask:0xf bound_ctrl:1
	v_mov_b32_e32 v75, v183
	s_mul_i32 s25, s34, 0x3000
	v_add_f32_dpp v18, v18, v18 row_mirror row_mask:0xf bank_mask:0xf bound_ctrl:1
	v_mov_b32_e32 v19, v18
	s_nop 1
	v_permlane16_swap_b32_e32 v18, v19
	v_add_f32_e32 v18, v18, v19
	v_mov_b32_e32 v19, v18
	s_nop 1
	v_permlane32_swap_b32_e32 v18, v19
	v_add_f32_e32 v18, v18, v19
	v_fmamk_f32 v18, v18, 0x3a800000, v225
	v_rsq_f32_e32 v90, v18
	ds_read_b128 v[18:21], v91 offset:4096
	ds_read_b128 v[22:25], v91 offset:8192
	v_lshl_add_u64 v[92:93], v[38:39], 0, s[2:3]
	v_pk_mul_f32 v[54:55], v[76:77], v[90:91] op_sel_hi:[1,0]
	v_pk_mul_f32 v[60:61], v[32:33], v[90:91] op_sel_hi:[1,0]
	s_waitcnt lgkmcnt(0)
	v_pk_fma_f32 v[66:67], v[18:19], v[54:55], v[22:23]
	ds_read_b128 v[26:29], v91 offset:5120
	ds_read_b128 v[30:33], v91 offset:9216
	v_med3_f32 v18, v66, s33, v226
	v_med3_f32 v19, v67, s33, v226
	v_cvt_pk_fp8_f32 v72, v18, v19
	v_pk_fma_f32 v[60:61], v[20:21], v[60:61], v[24:25]
	v_pk_mul_f32 v[20:21], v[82:83], v[90:91] op_sel_hi:[1,0]
	v_med3_f32 v18, v60, s33, v226
	v_med3_f32 v19, v61, s33, v226
	v_cvt_pk_fp8_f32 v72, v18, v19 op_sel:[0,0,1]
	v_pk_mul_f32 v[18:19], v[78:79], v[90:91] op_sel_hi:[1,0]
	s_waitcnt lgkmcnt(0)
	v_pk_fma_f32 v[32:33], v[28:29], v[20:21], v[32:33]
	v_pk_fma_f32 v[54:55], v[26:27], v[18:19], v[30:31]
	v_pk_mul_f32 v[26:27], v[84:85], v[90:91] op_sel_hi:[1,0]
	v_med3_f32 v18, v54, s33, v226
	v_med3_f32 v19, v55, s33, v226
	v_cvt_pk_fp8_f32 v73, v18, v19
	v_med3_f32 v18, v32, s33, v226
	v_med3_f32 v19, v33, s33, v226
	v_pk_mul_f32 v[30:31], v[80:81], v[90:91] op_sel_hi:[1,0]
	v_cvt_pk_fp8_f32 v73, v18, v19 op_sel:[0,0,1]
	ds_read_b128 v[18:21], v91 offset:6144
	ds_read_b128 v[22:25], v91 offset:10240
	ds_read_b128 v[76:79], v91 offset:7168
	ds_read_b128 v[80:83], v91 offset:11264
	v_add_u32_e32 v84, s25, v98
	s_ashr_i32 s25, s24, 31
	s_lshl_b64 s[2:3], s[24:25], 11
	s_waitcnt lgkmcnt(2)
	v_pk_fma_f32 v[28:29], v[26:27], v[18:19], v[22:23]
	v_mul_f32_e32 v26, v71, v71
	v_mul_f32_e32 v27, v69, v69
	v_fmac_f32_e32 v26, v70, v70
	v_fmac_f32_e32 v27, v68, v68
	v_pk_fma_f32 v[24:25], v[30:31], v[20:21], v[24:25]
	v_add_f32_e32 v26, v26, v27
	v_mul_f32_e32 v27, v65, v65
	v_mul_f32_e32 v30, v63, v63
	v_fmac_f32_e32 v27, v64, v64
	v_fmac_f32_e32 v30, v62, v62
	v_add_f32_e32 v27, v27, v30
	v_add_f32_e32 v26, v26, v27
	v_mul_f32_e32 v27, v59, v59
	v_mul_f32_e32 v30, v57, v57
	v_fmac_f32_e32 v27, v58, v58
	v_fmac_f32_e32 v30, v56, v56
	v_add_f32_e32 v27, v27, v30
	v_add_f32_e32 v26, v26, v27
	v_mul_f32_e32 v27, v53, v53
	v_mul_f32_e32 v30, v51, v51
	v_fmac_f32_e32 v27, v52, v52
	v_fmac_f32_e32 v30, v50, v50
	v_add_f32_e32 v27, v27, v30
	v_med3_f32 v18, v28, s33, v226
	v_med3_f32 v19, v29, s33, v226
	v_add_f32_e32 v26, v27, v26
	v_cvt_pk_fp8_f32 v74, v18, v19
	v_med3_f32 v18, v24, s33, v226
	v_add_f32_dpp v26, v26, v26 quad_perm:[1,0,3,2] row_mask:0xf bank_mask:0xf bound_ctrl:1
	v_med3_f32 v19, v25, s33, v226
	v_cvt_pk_fp8_f32 v74, v18, v19 op_sel:[0,0,1]
	v_add_f32_dpp v26, v26, v26 quad_perm:[2,3,0,1] row_mask:0xf bank_mask:0xf bound_ctrl:1
	v_pk_mul_f32 v[18:19], v[88:89], v[90:91] op_sel_hi:[1,0]
	v_pk_mul_f32 v[22:23], v[86:87], v[90:91] op_sel_hi:[1,0]
	v_add_f32_dpp v26, v26, v26 row_half_mirror row_mask:0xf bank_mask:0xf bound_ctrl:1
	s_waitcnt lgkmcnt(0)
	v_pk_fma_f32 v[20:21], v[18:19], v[76:77], v[80:81]
	v_add_f32_dpp v26, v26, v26 row_mirror row_mask:0xf bank_mask:0xf bound_ctrl:1
	v_mov_b32_e32 v27, v26
	s_nop 1
	v_permlane16_swap_b32_e32 v26, v27
	v_med3_f32 v18, v20, s33, v226
	v_med3_f32 v19, v21, s33, v226
	v_add_f32_e32 v26, v26, v27
	v_cvt_pk_fp8_f32 v75, v18, v19
	v_mov_b32_e32 v27, v26
	s_nop 1
	v_permlane32_swap_b32_e32 v26, v27
	v_pk_fma_f32 v[18:19], v[22:23], v[78:79], v[82:83]
	v_add_f32_e32 v26, v26, v27
	v_med3_f32 v22, v18, s33, v226
	v_med3_f32 v23, v19, s33, v226
	v_fmamk_f32 v26, v26, 0x3a800000, v225
	v_cvt_pk_fp8_f32 v75, v22, v23 op_sel:[0,0,1]
	v_rsq_f32_e32 v26, v26
	v_lshl_add_u64 v[22:23], s[80:81], 0, v[44:45]
	ds_read_b128 v[76:79], v84
	global_store_dwordx4 v[22:23], v[72:75], off
	v_pk_mul_f32 v[22:23], v[26:27], v[70:71] op_sel_hi:[0,1]
	v_pk_mul_f32 v[30:31], v[26:27], v[68:69] op_sel_hi:[0,1]
	ds_read_b128 v[68:71], v84 offset:1024
	s_waitcnt vmcnt(3) lgkmcnt(1)
; #define GAS __attribute__((address_space(1)))
; #define LAS __attribute__((address_space(3)))
; __device__ __forceinline__ float rsq(float x) { return __builtin_amdgcn_rsqf(x); }
; __device__ __forceinline__ void post_mix_front(Frame& F, int l, int m, const f32x4 (&y)[4], f32x4 (&x)[4], const LAS float* PV) {
;     const int lane = F.lane, b = m >> 12; const LAS f32x4* A = (const LAS f32x4*)(PV + b * 3072); const LAS f32x4* Bv = A + 256; const LAS f32x4* Cv = A + 512;
;     const float rstd = rsq(row_ss(y, lane) * (1.0f / DM) + EPS);
; #pragma unroll
;     for (int j = 0; j < 4; ++j) { const int c4 = lane + 64 * j; x[j] = x[j] + A[c4] * (y[j] * rstd); }
;     roww_store_bf16((GAS bf16*)(F.ws + WS_XR) + (size_t)m * DM, lane, x);
;     const float rstd2 = rsq(row_ss(x, lane) * (1.0f / DM) + EPS);
;     v4u hw;
; #pragma unroll
;     for (int j = 0; j < 4; ++j) { const int c4 = lane + 64 * j; x[j] = x[j] * rstd2 * Bv[c4] + Cv[c4]; hw[j] = pk4_f8(x[j][0], x[j][1], x[j][2], x[j][3]); }
;     ((GAS v4u*)((GAS unsigned char*)(F.ws + WS_HN) + (size_t)m * DM))[lane] = hw;
; }
; __device__ __forceinline__ void phase_post_mix(Frame& F, int l) {
;     ...
;     for (int m0 = gw; m0 < M; m0 += 4 * NGW) {
;         int mm[4]; f32x4 xx[4][4];
; #pragma unroll
;         for (int q = 0; q < 4; ++q) mm[q] = (m0 + q * NGW < M) ? m0 + q * NGW : m0;
; #pragma unroll
;         for (int q = 0; q < 4; q += 2) { f32x4 ya[4], yb[4];
;             roww_load_bf16(Y + (size_t)mm[q] * DM, lane, ya); roww_load_bf16(Y + (size_t)mm[q + 1] * DM, lane, yb);
;             if (l == 0) { roww_load(xin + (size_t)mm[q] * DM, lane, xx[q]); roww_load(xin + (size_t)mm[q + 1] * DM, lane, xx[q + 1]); }
;             else { roww_load_bf16(xr + (size_t)mm[q] * DM, lane, xx[q]); roww_load_bf16(xr + (size_t)mm[q + 1] * DM, lane, xx[q + 1]); }
;             post_mix_front(F, l, mm[q], ya, xx[q], PV); post_mix_front(F, l, mm[q + 1], yb, xx[q + 1], PV); }
	v_pk_fma_f32 v[22:23], v[76:77], v[22:23], v[14:15]
	v_pk_mul_f32 v[14:15], v[26:27], v[62:63] op_sel_hi:[0,1]
	v_pk_fma_f32 v[30:31], v[78:79], v[30:31], v[16:17]
	v_pk_mul_f32 v[16:17], v[26:27], v[64:65] op_sel_hi:[0,1]
	s_waitcnt lgkmcnt(0)
	v_pk_fma_f32 v[62:63], v[70:71], v[14:15], v[12:13]
	ds_read_b128 v[12:15], v84 offset:2048
	v_pk_fma_f32 v[64:65], v[68:69], v[16:17], v[10:11]
	v_pk_mul_f32 v[10:11], v[26:27], v[58:59] op_sel_hi:[0,1]
	v_pk_mul_f32 v[16:17], v[26:27], v[56:57] op_sel_hi:[0,1]
	ds_read_b128 v[56:59], v84 offset:3072
	s_waitcnt lgkmcnt(1)
	v_pk_fma_f32 v[72:73], v[12:13], v[10:11], v[6:7]
	v_mul_f32_e32 v10, v23, v23
	v_mul_f32_e32 v11, v31, v31
	v_fmac_f32_e32 v10, v22, v22
	v_fmac_f32_e32 v11, v30, v30
	v_add_f32_e32 v10, v10, v11
	v_mul_f32_e32 v11, v65, v65
	v_mul_f32_e32 v12, v63, v63
	v_fmac_f32_e32 v11, v64, v64
	v_fmac_f32_e32 v12, v62, v62
	v_pk_fma_f32 v[68:69], v[14:15], v[16:17], v[8:9]
	v_add_f32_e32 v11, v11, v12
	v_add_f32_e32 v10, v10, v11
	v_mul_f32_e32 v11, v73, v73
	v_mul_f32_e32 v12, v69, v69
	v_pk_mul_f32 v[6:7], v[26:27], v[52:53] op_sel_hi:[0,1]
	v_pk_mul_f32 v[8:9], v[26:27], v[50:51] op_sel_hi:[0,1]
	v_fmac_f32_e32 v11, v72, v72
	v_fmac_f32_e32 v12, v68, v68
	s_waitcnt lgkmcnt(0)
	v_pk_fma_f32 v[26:27], v[58:59], v[8:9], v[4:5]
	v_pk_fma_f32 v[88:89], v[56:57], v[6:7], v[2:3]
	v_add_f32_e32 v11, v11, v12
	v_add_f32_e32 v10, v11, v10
	v_mul_f32_e32 v11, v89, v89
	v_mul_f32_e32 v12, v27, v27
	v_fmac_f32_e32 v11, v88, v88
	v_fmac_f32_e32 v12, v26, v26
	v_add_f32_e32 v11, v11, v12
	v_add_f32_e32 v10, v11, v10
	v_cvt_pk_bf16_f32 v2, v22, v23
	v_cvt_pk_bf16_f32 v3, v30, v31
	v_add_f32_dpp v10, v10, v10 quad_perm:[1,0,3,2] row_mask:0xf bank_mask:0xf bound_ctrl:1
	v_cvt_pk_bf16_f32 v4, v64, v65
	v_cvt_pk_bf16_f32 v9, v26, v27
	v_add_f32_dpp v10, v10, v10 quad_perm:[2,3,0,1] row_mask:0xf bank_mask:0xf bound_ctrl:1
	v_cvt_pk_bf16_f32 v5, v62, v63
	v_cvt_pk_bf16_f32 v6, v72, v73
	v_add_f32_dpp v10, v10, v10 row_half_mirror row_mask:0xf bank_mask:0xf bound_ctrl:1
	v_cvt_pk_bf16_f32 v7, v68, v69
	v_cvt_pk_bf16_f32 v8, v88, v89
	v_add_f32_dpp v10, v10, v10 row_mirror row_mask:0xf bank_mask:0xf bound_ctrl:1
	v_mov_b32_e32 v11, v10
	s_nop 1
	v_permlane16_swap_b32_e32 v10, v11
	v_add_f32_e32 v10, v10, v11
	v_mov_b32_e32 v11, v10
	s_nop 1
	v_permlane32_swap_b32_e32 v10, v11
	v_add_f32_e32 v10, v10, v11
	v_fmamk_f32 v10, v10, 0x3a800000, v225
	v_rsq_f32_e32 v90, v10
	ds_read_b128 v[10:13], v84 offset:4096
	ds_read_b128 v[14:17], v84 offset:8192
	ds_read_b128 v[50:53], v84 offset:5120
	ds_read_b128 v[56:59], v84 offset:9216
	v_pk_mul_f32 v[22:23], v[22:23], v[90:91] op_sel_hi:[1,0]
	v_pk_mul_f32 v[30:31], v[30:31], v[90:91] op_sel_hi:[1,0]
	s_waitcnt lgkmcnt(2)
	v_pk_fma_f32 v[74:75], v[10:11], v[22:23], v[14:15]
	v_mov_b32_e32 v10, v183
	v_med3_f32 v11, v74, s33, v226
	v_med3_f32 v14, v75, s33, v226
	v_cvt_pk_fp8_f32 v10, v11, v14
	v_pk_fma_f32 v[70:71], v[12:13], v[30:31], v[16:17]
	v_pk_mul_f32 v[14:15], v[62:63], v[90:91] op_sel_hi:[1,0]
	v_med3_f32 v11, v70, s33, v226
	v_med3_f32 v12, v71, s33, v226
	v_cvt_pk_fp8_f32 v10, v11, v12 op_sel:[0,0,1]
	v_pk_mul_f32 v[12:13], v[64:65], v[90:91] op_sel_hi:[1,0]
	v_mov_b32_e32 v11, v183
	s_waitcnt lgkmcnt(0)
	v_pk_fma_f32 v[64:65], v[50:51], v[12:13], v[56:57]
	v_pk_fma_f32 v[58:59], v[52:53], v[14:15], v[58:59]
	v_med3_f32 v12, v64, s33, v226
	v_med3_f32 v13, v65, s33, v226
	v_cvt_pk_fp8_f32 v11, v12, v13
	v_med3_f32 v12, v58, s33, v226
	v_med3_f32 v13, v59, s33, v226
	v_pk_mul_f32 v[16:17], v[72:73], v[90:91] op_sel_hi:[1,0]
	v_cvt_pk_fp8_f32 v11, v12, v13 op_sel:[0,0,1]
	ds_read_b128 v[12:15], v84 offset:6144
	ds_read_b128 v[76:79], v84 offset:10240
	ds_read_b128 v[80:83], v84 offset:7168
	ds_read_b128 v[84:87], v84 offset:11264
	v_pk_mul_f32 v[22:23], v[68:69], v[90:91] op_sel_hi:[1,0]
	global_store_dwordx4 v[92:93], v[2:5], off
	global_store_dwordx4 v[92:93], v[6:9], off offset:16
	s_waitcnt lgkmcnt(2)
	v_pk_fma_f32 v[52:53], v[16:17], v[12:13], v[76:77]
	s_nop 0
	v_med3_f32 v13, v52, s33, v226
	v_med3_f32 v16, v53, s33, v226
	v_mov_b32_e32 v12, v183
	v_cvt_pk_fp8_f32 v12, v13, v16
	v_pk_fma_f32 v[30:31], v[22:23], v[14:15], v[78:79]
	v_pk_mul_f32 v[16:17], v[26:27], v[90:91] op_sel_hi:[1,0]
	v_med3_f32 v13, v30, s33, v226
	v_med3_f32 v14, v31, s33, v226
	v_cvt_pk_fp8_f32 v12, v13, v14 op_sel:[0,0,1]
	v_pk_mul_f32 v[14:15], v[88:89], v[90:91] op_sel_hi:[1,0]
	v_mov_b32_e32 v13, v183
	s_waitcnt lgkmcnt(0)
	v_pk_fma_f32 v[26:27], v[14:15], v[80:81], v[84:85]
	v_pk_fma_f32 v[22:23], v[16:17], v[82:83], v[86:87]
	v_med3_f32 v14, v26, s33, v226
	v_med3_f32 v15, v27, s33, v226
	v_cvt_pk_fp8_f32 v13, v14, v15
	v_med3_f32 v14, v22, s33, v226
	v_med3_f32 v15, v23, s33, v226
	v_lshl_add_u64 v[2:3], v[40:41], 0, s[36:37]
	v_cvt_pk_fp8_f32 v13, v14, v15 op_sel:[0,0,1]
	v_lshl_add_u64 v[6:7], v[34:35], 0, s[38:39]
	v_lshl_add_u64 v[14:15], v[34:35], 0, s[2:3]
	s_lshl_b64 s[36:37], s[26:27], 12
	global_store_dwordx4 v[2:3], v[10:13], off
	global_load_dwordx4 v[2:5], v[6:7], off
	s_nop 0
	global_load_dwordx4 v[6:9], v[6:7], off offset:16
	s_nop 0
	global_load_dwordx4 v[10:13], v[14:15], off
	s_nop 0
	global_load_dwordx4 v[14:17], v[14:15], off offset:16
	s_waitcnt vmcnt(3)
	v_lshlrev_b32_e32 v50, 16, v2
	v_and_b32_e32 v51, 0xffff0000, v2
	v_lshlrev_b32_e32 v56, 16, v3
	v_and_b32_e32 v57, 0xffff0000, v3
	v_lshl_add_u64 v[2:3], v[36:37], 0, s[36:37]
	global_load_dwordx4 v[76:79], v[2:3], off offset:16
	global_load_dwordx4 v[100:103], v[2:3], off
	global_load_dwordx4 v[104:107], v[2:3], off offset:48
	global_load_dwordx4 v[108:111], v[2:3], off offset:32
	s_waitcnt vmcnt(5)
; #define GAS __attribute__((address_space(1)))
; #define LAS __attribute__((address_space(3)))
; __device__ __forceinline__ float rsq(float x) { return __builtin_amdgcn_rsqf(x); }
; __device__ __forceinline__ void post_mix_front(Frame& F, int l, int m, const f32x4 (&y)[4], f32x4 (&x)[4], const LAS float* PV) {
;     const int lane = F.lane, b = m >> 12; const LAS f32x4* A = (const LAS f32x4*)(PV + b * 3072); const LAS f32x4* Bv = A + 256; const LAS f32x4* Cv = A + 512;
;     const float rstd = rsq(row_ss(y, lane) * (1.0f / DM) + EPS);
; #pragma unroll
;     for (int j = 0; j < 4; ++j) { const int c4 = lane + 64 * j; x[j] = x[j] + A[c4] * (y[j] * rstd); }
;     roww_store_bf16((GAS bf16*)(F.ws + WS_XR) + (size_t)m * DM, lane, x);
;     const float rstd2 = rsq(row_ss(x, lane) * (1.0f / DM) + EPS);
;     v4u hw;
; #pragma unroll
;     for (int j = 0; j < 4; ++j) { const int c4 = lane + 64 * j; x[j] = x[j] * rstd2 * Bv[c4] + Cv[c4]; hw[j] = pk4_f8(x[j][0], x[j][1], x[j][2], x[j][3]); }
;     ((GAS v4u*)((GAS unsigned char*)(F.ws + WS_HN) + (size_t)m * DM))[lane] = hw;
; }
; __device__ __forceinline__ void phase_post_mix(Frame& F, int l) {
;     ...
;         for (int q = 0; q < 4; q += 2) { f32x4 ya[4], yb[4];
;             roww_load_bf16(Y + (size_t)mm[q] * DM, lane, ya); roww_load_bf16(Y + (size_t)mm[q + 1] * DM, lane, yb);
;             if (l == 0) { roww_load(xin + (size_t)mm[q] * DM, lane, xx[q]); roww_load(xin + (size_t)mm[q + 1] * DM, lane, xx[q + 1]); }
;             else { roww_load_bf16(xr + (size_t)mm[q] * DM, lane, xx[q]); roww_load_bf16(xr + (size_t)mm[q + 1] * DM, lane, xx[q + 1]); }
;             post_mix_front(F, l, mm[q], ya, xx[q], PV); post_mix_front(F, l, mm[q + 1], yb, xx[q + 1], PV); }
	v_lshlrev_b32_e32 v96, 16, v10
	v_and_b32_e32 v97, 0xffff0000, v10
	v_lshlrev_b32_e32 v94, 16, v11
	v_and_b32_e32 v95, 0xffff0000, v11
	v_mul_f32_e32 v10, v51, v51
	v_mul_f32_e32 v11, v57, v57
	v_and_b32_e32 v63, 0xffff0000, v4
	v_and_b32_e32 v69, 0xffff0000, v5
	v_fmac_f32_e32 v10, v50, v50
	v_fmac_f32_e32 v11, v56, v56
	v_lshlrev_b32_e32 v62, 16, v4
	v_lshlrev_b32_e32 v68, 16, v5
	v_lshlrev_b32_e32 v92, 16, v12
	v_and_b32_e32 v93, 0xffff0000, v12
	v_add_f32_e32 v10, v10, v11
	v_mul_f32_e32 v11, v63, v63
	v_mul_f32_e32 v12, v69, v69
	v_fmac_f32_e32 v11, v62, v62
	v_fmac_f32_e32 v12, v68, v68
	v_and_b32_e32 v73, 0xffff0000, v6
	v_and_b32_e32 v121, 0xffff0000, v7
	v_add_f32_e32 v11, v11, v12
	v_lshlrev_b32_e32 v72, 16, v6
	v_lshlrev_b32_e32 v120, 16, v7
	v_add_f32_e32 v10, v10, v11
	v_mul_f32_e32 v11, v73, v73
	v_mul_f32_e32 v12, v121, v121
	v_fmac_f32_e32 v11, v72, v72
	v_fmac_f32_e32 v12, v120, v120
	v_and_b32_e32 v123, 0xffff0000, v8
	v_and_b32_e32 v125, 0xffff0000, v9
	v_add_f32_e32 v11, v11, v12
	v_lshlrev_b32_e32 v122, 16, v8
	v_lshlrev_b32_e32 v124, 16, v9
	v_add_f32_e32 v10, v10, v11
	v_mul_f32_e32 v11, v123, v123
	v_mul_f32_e32 v12, v125, v125
	v_fmac_f32_e32 v11, v122, v122
	v_fmac_f32_e32 v12, v124, v124
	v_add_f32_e32 v11, v11, v12
	v_add_f32_e32 v10, v11, v10
	s_lshl_b64 s[36:37], s[24:25], 12
	s_waitcnt vmcnt(4)
	v_lshlrev_b32_e32 v88, 16, v14
	v_add_f32_dpp v10, v10, v10 quad_perm:[1,0,3,2] row_mask:0xf bank_mask:0xf bound_ctrl:1
	v_and_b32_e32 v89, 0xffff0000, v14
	v_lshlrev_b32_e32 v86, 16, v15
	v_add_f32_dpp v10, v10, v10 quad_perm:[2,3,0,1] row_mask:0xf bank_mask:0xf bound_ctrl:1
	v_and_b32_e32 v87, 0xffff0000, v15
	v_lshl_add_u64 v[14:15], v[36:37], 0, s[36:37]
	v_add_f32_dpp v10, v10, v10 row_half_mirror row_mask:0xf bank_mask:0xf bound_ctrl:1
	s_ashr_i32 s36, s26, 12
	s_mul_i32 s29, s36, 0x3000
	v_add_f32_dpp v10, v10, v10 row_mirror row_mask:0xf bank_mask:0xf bound_ctrl:1
	v_mov_b32_e32 v11, v10
	s_nop 1
	v_permlane16_swap_b32_e32 v10, v11
	v_add_f32_e32 v10, v10, v11
	v_mov_b32_e32 v11, v10
	s_nop 1
	v_permlane32_swap_b32_e32 v10, v11
	v_add_f32_e32 v10, v10, v11
	v_fmamk_f32 v10, v10, 0x3a800000, v225
	v_add_u32_e32 v99, s29, v98
	v_lshlrev_b32_e32 v90, 16, v13
	v_and_b32_e32 v91, 0xffff0000, v13
	v_lshlrev_b32_e32 v84, 16, v16
	v_and_b32_e32 v85, 0xffff0000, v16
	v_lshlrev_b32_e32 v82, 16, v17
	v_and_b32_e32 v83, 0xffff0000, v17
	global_load_dwordx4 v[2:5], v[14:15], off offset:48
	global_load_dwordx4 v[6:9], v[14:15], off offset:32
	v_rsq_f32_e32 v126, v10
	ds_read_b128 v[112:115], v99
	global_load_dwordx4 v[10:13], v[14:15], off offset:16
	s_nop 0
	global_load_dwordx4 v[14:17], v[14:15], off
	ds_read_b128 v[116:119], v99 offset:1024
	v_pk_mul_f32 v[50:51], v[126:127], v[50:51] op_sel_hi:[0,1]
	v_pk_mul_f32 v[56:57], v[126:127], v[56:57] op_sel_hi:[0,1]
	v_pk_mul_f32 v[68:69], v[126:127], v[68:69] op_sel_hi:[0,1]
	v_pk_mul_f32 v[62:63], v[126:127], v[62:63] op_sel_hi:[0,1]
	s_waitcnt vmcnt(6) lgkmcnt(1)
	v_pk_fma_f32 v[56:57], v[114:115], v[56:57], v[102:103]
	v_pk_fma_f32 v[50:51], v[112:113], v[50:51], v[100:101]
	ds_read_b128 v[100:103], v99 offset:3072
	s_waitcnt lgkmcnt(1)
	v_pk_fma_f32 v[68:69], v[118:119], v[68:69], v[78:79]
	ds_read_b128 v[78:81], v99 offset:2048
	v_pk_fma_f32 v[62:63], v[116:117], v[62:63], v[76:77]
	v_pk_mul_f32 v[72:73], v[126:127], v[72:73] op_sel_hi:[0,1]
	v_pk_mul_f32 v[76:77], v[126:127], v[120:121] op_sel_hi:[0,1]
	s_waitcnt vmcnt(4) lgkmcnt(0)
	v_pk_fma_f32 v[112:113], v[80:81], v[76:77], v[110:111]
	v_pk_fma_f32 v[114:115], v[78:79], v[72:73], v[108:109]
	v_pk_mul_f32 v[72:73], v[126:127], v[122:123] op_sel_hi:[0,1]
	v_pk_mul_f32 v[76:77], v[126:127], v[124:125] op_sel_hi:[0,1]
	v_pk_fma_f32 v[118:119], v[102:103], v[76:77], v[106:107]
	v_pk_fma_f32 v[120:121], v[100:101], v[72:73], v[104:105]
	v_cvt_pk_bf16_f32 v76, v50, v51
	v_cvt_pk_bf16_f32 v77, v56, v57
	v_cvt_pk_bf16_f32 v78, v62, v63
	v_cvt_pk_bf16_f32 v79, v68, v69
	v_lshl_add_u64 v[72:73], v[38:39], 0, s[38:39]
	global_store_dwordx4 v[72:73], v[76:79], off
	v_cvt_pk_bf16_f32 v100, v114, v115
	v_cvt_pk_bf16_f32 v101, v112, v113
	v_mul_f32_e32 v76, v51, v51
	v_mul_f32_e32 v77, v57, v57
	v_fmac_f32_e32 v76, v50, v50
	v_fmac_f32_e32 v77, v56, v56
	v_add_f32_e32 v76, v76, v77
	v_mul_f32_e32 v77, v63, v63
	v_mul_f32_e32 v78, v69, v69
	v_fmac_f32_e32 v77, v62, v62
	v_fmac_f32_e32 v78, v68, v68
	v_add_f32_e32 v77, v77, v78
	v_add_f32_e32 v76, v76, v77
	v_mul_f32_e32 v77, v115, v115
	v_mul_f32_e32 v78, v113, v113
	v_fmac_f32_e32 v77, v114, v114
	v_fmac_f32_e32 v78, v112, v112
	v_add_f32_e32 v77, v77, v78
	v_add_f32_e32 v76, v77, v76
	v_mul_f32_e32 v77, v121, v121
	v_mul_f32_e32 v78, v119, v119
	v_fmac_f32_e32 v77, v120, v120
	v_fmac_f32_e32 v78, v118, v118
	v_add_f32_e32 v77, v77, v78
	v_add_f32_e32 v76, v77, v76
	v_cvt_pk_bf16_f32 v102, v120, v121
	v_cvt_pk_bf16_f32 v103, v118, v119
	v_add_f32_dpp v76, v76, v76 quad_perm:[1,0,3,2] row_mask:0xf bank_mask:0xf bound_ctrl:1
	global_store_dwordx4 v[72:73], v[100:103], off offset:16
	s_ashr_i32 s38, s24, 12
	v_add_f32_dpp v76, v76, v76 quad_perm:[2,3,0,1] row_mask:0xf bank_mask:0xf bound_ctrl:1
	s_mul_i32 s27, s38, 0x3000
	s_nop 0
	v_add_f32_dpp v76, v76, v76 row_half_mirror row_mask:0xf bank_mask:0xf bound_ctrl:1
	s_nop 1
	v_add_f32_dpp v76, v76, v76 row_mirror row_mask:0xf bank_mask:0xf bound_ctrl:1
	v_mov_b32_e32 v77, v76
	s_nop 1
	v_permlane16_swap_b32_e32 v76, v77
	v_add_f32_e32 v76, v76, v77
	v_mov_b32_e32 v77, v76
	s_nop 1
	v_permlane32_swap_b32_e32 v76, v77
	v_add_f32_e32 v76, v76, v77
	v_fmamk_f32 v76, v76, 0x3a800000, v225
	v_rsq_f32_e32 v122, v76
	ds_read_b128 v[76:79], v99 offset:4096
	ds_read_b128 v[100:103], v99 offset:8192
	ds_read_b128 v[104:107], v99 offset:5120
	ds_read_b128 v[108:111], v99 offset:9216
	v_pk_mul_f32 v[50:51], v[50:51], v[122:123] op_sel_hi:[1,0]
	v_pk_mul_f32 v[56:57], v[56:57], v[122:123] op_sel_hi:[1,0]
	s_waitcnt lgkmcnt(2)
; #define GAS __attribute__((address_space(1)))
; #define LAS __attribute__((address_space(3)))
; __device__ __forceinline__ float rsq(float x) { return __builtin_amdgcn_rsqf(x); }
; __device__ __forceinline__ void post_mix_front(Frame& F, int l, int m, const f32x4 (&y)[4], f32x4 (&x)[4], const LAS float* PV) {
;     const int lane = F.lane, b = m >> 12; const LAS f32x4* A = (const LAS f32x4*)(PV + b * 3072); const LAS f32x4* Bv = A + 256; const LAS f32x4* Cv = A + 512;
;     const float rstd = rsq(row_ss(y, lane) * (1.0f / DM) + EPS);
; #pragma unroll
;     for (int j = 0; j < 4; ++j) { const int c4 = lane + 64 * j; x[j] = x[j] + A[c4] * (y[j] * rstd); }
;     roww_store_bf16((GAS bf16*)(F.ws + WS_XR) + (size_t)m * DM, lane, x);
;     const float rstd2 = rsq(row_ss(x, lane) * (1.0f / DM) + EPS);
;     v4u hw;
; #pragma unroll
;     for (int j = 0; j < 4; ++j) { const int c4 = lane + 64 * j; x[j] = x[j] * rstd2 * Bv[c4] + Cv[c4]; hw[j] = pk4_f8(x[j][0], x[j][1], x[j][2], x[j][3]); }
;     ((GAS v4u*)((GAS unsigned char*)(F.ws + WS_HN) + (size_t)m * DM))[lane] = hw;
; }
	v_pk_fma_f32 v[80:81], v[76:77], v[50:51], v[100:101]
	v_mov_b32_e32 v100, v183
	v_med3_f32 v50, v80, s33, v226
	v_med3_f32 v51, v81, s33, v226
	v_cvt_pk_fp8_f32 v100, v50, v51
	v_pk_fma_f32 v[78:79], v[78:79], v[56:57], v[102:103]
	v_pk_mul_f32 v[56:57], v[68:69], v[122:123] op_sel_hi:[1,0]
	v_med3_f32 v50, v78, s33, v226
	v_med3_f32 v51, v79, s33, v226
	v_cvt_pk_fp8_f32 v100, v50, v51 op_sel:[0,0,1]
	v_pk_mul_f32 v[50:51], v[62:63], v[122:123] op_sel_hi:[1,0]
	v_mov_b32_e32 v101, v183
	s_waitcnt lgkmcnt(0)
	v_pk_fma_f32 v[76:77], v[104:105], v[50:51], v[108:109]
	v_pk_fma_f32 v[72:73], v[106:107], v[56:57], v[110:111]
	v_med3_f32 v50, v76, s33, v226
	v_med3_f32 v51, v77, s33, v226
	v_cvt_pk_fp8_f32 v101, v50, v51
	ds_read_b128 v[102:105], v99 offset:6144
	ds_read_b128 v[106:109], v99 offset:10240
	v_med3_f32 v50, v72, s33, v226
	v_med3_f32 v51, v73, s33, v226
	v_cvt_pk_fp8_f32 v101, v50, v51 op_sel:[0,0,1]
	v_pk_mul_f32 v[50:51], v[114:115], v[122:123] op_sel_hi:[1,0]
	v_pk_mul_f32 v[56:57], v[112:113], v[122:123] op_sel_hi:[1,0]
	s_waitcnt lgkmcnt(0)
	v_pk_fma_f32 v[68:69], v[50:51], v[102:103], v[106:107]
	v_mov_b32_e32 v102, v183
	v_med3_f32 v50, v68, s33, v226
	v_med3_f32 v51, v69, s33, v226
	ds_read_b128 v[110:113], v99 offset:7168
	ds_read_b128 v[114:117], v99 offset:11264
	v_cvt_pk_fp8_f32 v102, v50, v51
	v_pk_fma_f32 v[62:63], v[56:57], v[104:105], v[108:109]
	v_mov_b32_e32 v103, v183
	v_med3_f32 v50, v62, s33, v226
	v_med3_f32 v51, v63, s33, v226
	v_cvt_pk_fp8_f32 v102, v50, v51 op_sel:[0,0,1]
	v_pk_mul_f32 v[50:51], v[120:121], v[122:123] op_sel_hi:[1,0]
	v_pk_mul_f32 v[104:105], v[118:119], v[122:123] op_sel_hi:[1,0]
	s_waitcnt lgkmcnt(0)
	v_pk_fma_f32 v[56:57], v[50:51], v[110:111], v[114:115]
	v_lshl_add_u64 v[108:109], v[40:41], 0, s[40:41]
	v_med3_f32 v50, v56, s33, v226
	v_med3_f32 v51, v57, s33, v226
	v_cvt_pk_fp8_f32 v103, v50, v51
	v_pk_fma_f32 v[50:51], v[104:105], v[112:113], v[116:117]
	v_mul_f32_e32 v105, v91, v91
	v_med3_f32 v99, v50, s33, v226
	v_med3_f32 v104, v51, s33, v226
	v_cvt_pk_fp8_f32 v103, v99, v104 op_sel:[0,0,1]
	v_mul_f32_e32 v99, v97, v97
	v_mul_f32_e32 v104, v95, v95
	v_fmac_f32_e32 v99, v96, v96
	v_fmac_f32_e32 v104, v94, v94
	v_add_f32_e32 v99, v99, v104
	v_mul_f32_e32 v104, v93, v93
	v_fmac_f32_e32 v104, v92, v92
	v_fmac_f32_e32 v105, v90, v90
	v_add_f32_e32 v104, v104, v105
	v_add_f32_e32 v99, v99, v104
	v_mul_f32_e32 v104, v89, v89
	v_mul_f32_e32 v105, v87, v87
	v_fmac_f32_e32 v104, v88, v88
	v_fmac_f32_e32 v105, v86, v86
	v_add_f32_e32 v104, v104, v105
	v_add_f32_e32 v99, v99, v104
	v_mul_f32_e32 v104, v85, v85
	v_mul_f32_e32 v105, v83, v83
	v_fmac_f32_e32 v104, v84, v84
	v_fmac_f32_e32 v105, v82, v82
	v_add_f32_e32 v104, v104, v105
	v_add_f32_e32 v99, v104, v99
	global_store_dwordx4 v[108:109], v[100:103], off
	s_lshl_b64 s[40:41], s[24:25], 10
	v_add_f32_dpp v99, v99, v99 quad_perm:[1,0,3,2] row_mask:0xf bank_mask:0xf bound_ctrl:1
	s_nop 1
	v_add_f32_dpp v99, v99, v99 quad_perm:[2,3,0,1] row_mask:0xf bank_mask:0xf bound_ctrl:1
	s_nop 1
	v_add_f32_dpp v99, v99, v99 row_half_mirror row_mask:0xf bank_mask:0xf bound_ctrl:1
	s_nop 1
	v_add_f32_dpp v99, v99, v99 row_mirror row_mask:0xf bank_mask:0xf bound_ctrl:1
	v_mov_b32_e32 v104, v99
	s_nop 1
	v_permlane16_swap_b32_e32 v99, v104
	v_add_f32_e32 v99, v99, v104
	v_mov_b32_e32 v104, v99
	s_nop 1
	v_permlane32_swap_b32_e32 v99, v104
	v_add_f32_e32 v99, v99, v104
	v_fmamk_f32 v99, v99, 0x3a800000, v225
	v_rsq_f32_e32 v110, v99
	v_add_u32_e32 v99, s27, v98
	ds_read_b128 v[104:107], v99
	v_pk_mul_f32 v[100:101], v[110:111], v[96:97] op_sel_hi:[0,1]
	v_pk_mul_f32 v[102:103], v[110:111], v[94:95] op_sel_hi:[0,1]
	ds_read_b128 v[94:97], v99 offset:1024
	s_waitcnt vmcnt(3) lgkmcnt(1)
	v_pk_fma_f32 v[100:101], v[104:105], v[100:101], v[14:15]
	v_pk_mul_f32 v[14:15], v[110:111], v[90:91] op_sel_hi:[0,1]
	v_pk_mul_f32 v[92:93], v[110:111], v[92:93] op_sel_hi:[0,1]
	v_pk_mul_f32 v[90:91], v[110:111], v[88:89] op_sel_hi:[0,1]
	s_waitcnt lgkmcnt(0)
	v_pk_fma_f32 v[96:97], v[96:97], v[14:15], v[12:13]
	ds_read_b128 v[12:15], v99 offset:2048
	v_pk_fma_f32 v[10:11], v[94:95], v[92:93], v[10:11]
	v_pk_mul_f32 v[92:93], v[110:111], v[86:87] op_sel_hi:[0,1]
	ds_read_b128 v[86:89], v99 offset:3072
	v_pk_fma_f32 v[16:17], v[106:107], v[102:103], v[16:17]
	s_waitcnt lgkmcnt(1)
	v_pk_fma_f32 v[104:105], v[12:13], v[90:91], v[6:7]
	v_pk_mul_f32 v[6:7], v[110:111], v[84:85] op_sel_hi:[0,1]
	v_pk_fma_f32 v[102:103], v[14:15], v[92:93], v[8:9]
	s_waitcnt lgkmcnt(0)
	v_pk_fma_f32 v[108:109], v[86:87], v[6:7], v[2:3]
	v_mul_f32_e32 v6, v101, v101
	v_mul_f32_e32 v7, v17, v17
	v_pk_mul_f32 v[8:9], v[110:111], v[82:83] op_sel_hi:[0,1]
	v_fmac_f32_e32 v6, v100, v100
	v_fmac_f32_e32 v7, v16, v16
	v_pk_fma_f32 v[106:107], v[88:89], v[8:9], v[4:5]
	v_add_f32_e32 v6, v6, v7
	v_mul_f32_e32 v7, v11, v11
	v_mul_f32_e32 v8, v97, v97
	v_fmac_f32_e32 v7, v10, v10
	v_fmac_f32_e32 v8, v96, v96
	v_add_f32_e32 v7, v7, v8
	v_add_f32_e32 v6, v6, v7
	v_mul_f32_e32 v7, v105, v105
	v_mul_f32_e32 v8, v103, v103
	v_fmac_f32_e32 v7, v104, v104
	v_fmac_f32_e32 v8, v102, v102
	v_add_f32_e32 v7, v7, v8
	v_add_f32_e32 v6, v7, v6
	v_mul_f32_e32 v7, v109, v109
	v_mul_f32_e32 v8, v107, v107
	v_fmac_f32_e32 v7, v108, v108
	v_fmac_f32_e32 v8, v106, v106
	v_add_f32_e32 v7, v7, v8
	v_add_f32_e32 v6, v7, v6
	v_cvt_pk_bf16_f32 v2, v100, v101
	v_cvt_pk_bf16_f32 v3, v16, v17
	v_add_f32_dpp v6, v6, v6 quad_perm:[1,0,3,2] row_mask:0xf bank_mask:0xf bound_ctrl:1
	v_cvt_pk_bf16_f32 v4, v10, v11
	v_cvt_pk_bf16_f32 v5, v96, v97
	v_add_f32_dpp v6, v6, v6 quad_perm:[2,3,0,1] row_mask:0xf bank_mask:0xf bound_ctrl:1
	v_lshl_add_u64 v[110:111], v[38:39], 0, s[2:3]
	global_store_dwordx4 v[110:111], v[2:5], off
	v_add_f32_dpp v6, v6, v6 row_half_mirror row_mask:0xf bank_mask:0xf bound_ctrl:1
	v_mov_b32_e32 v94, v183
	v_mov_b32_e32 v95, v183
	v_add_f32_dpp v6, v6, v6 row_mirror row_mask:0xf bank_mask:0xf bound_ctrl:1
	v_mov_b32_e32 v7, v6
	s_nop 1
	v_permlane16_swap_b32_e32 v6, v7
	v_add_f32_e32 v6, v6, v7
	v_mov_b32_e32 v7, v6
	s_nop 1
	v_permlane32_swap_b32_e32 v6, v7
	v_add_f32_e32 v6, v6, v7
	v_fmamk_f32 v6, v6, 0x3a800000, v225
	v_rsq_f32_e32 v112, v6
	ds_read_b128 v[2:5], v99 offset:4096
	ds_read_b128 v[6:9], v99 offset:8192
	ds_read_b128 v[86:89], v99 offset:5120
	ds_read_b128 v[90:93], v99 offset:9216
	v_cvt_pk_bf16_f32 v82, v104, v105
	v_pk_mul_f32 v[12:13], v[100:101], v[112:113] op_sel_hi:[1,0]
	v_pk_mul_f32 v[14:15], v[16:17], v[112:113] op_sel_hi:[1,0]
	s_waitcnt lgkmcnt(2)
; #define GAS __attribute__((address_space(1)))
; #define LAS __attribute__((address_space(3)))
; __device__ __forceinline__ float rsq(float x) { return __builtin_amdgcn_rsqf(x); }
; __device__ __forceinline__ void post_mix_front(Frame& F, int l, int m, const f32x4 (&y)[4], f32x4 (&x)[4], const LAS float* PV) {
;     const int lane = F.lane, b = m >> 12; const LAS f32x4* A = (const LAS f32x4*)(PV + b * 3072); const LAS f32x4* Bv = A + 256; const LAS f32x4* Cv = A + 512;
;     const float rstd = rsq(row_ss(y, lane) * (1.0f / DM) + EPS);
; #pragma unroll
;     for (int j = 0; j < 4; ++j) { const int c4 = lane + 64 * j; x[j] = x[j] + A[c4] * (y[j] * rstd); }
;     roww_store_bf16((GAS bf16*)(F.ws + WS_XR) + (size_t)m * DM, lane, x);
;     const float rstd2 = rsq(row_ss(x, lane) * (1.0f / DM) + EPS);
;     v4u hw;
; #pragma unroll
;     for (int j = 0; j < 4; ++j) { const int c4 = lane + 64 * j; x[j] = x[j] * rstd2 * Bv[c4] + Cv[c4]; hw[j] = pk4_f8(x[j][0], x[j][1], x[j][2], x[j][3]); }
;     ((GAS v4u*)((GAS unsigned char*)(F.ws + WS_HN) + (size_t)m * DM))[lane] = hw;
; }
; __device__ __forceinline__ void phase_post_mix(Frame& F, int l) {
;     ...
;         for (int j = 0; j < 4; ++j) { const LAS float* wg = rws + (lane + 64 * j) * 68;
; #pragma unroll
;             for (int i = 0; i < 4; ++i) { const f32x4 w0 = *(const LAS f32x4*)(wg + 16 * i), w1 = *(const LAS f32x4*)(wg + 16 * i + 4), w2 = *(const LAS f32x4*)(wg + 16 * i + 8), w3 = *(const LAS f32x4*)(wg + 16 * i + 12);
;                 const r_f32x2 wv[8] = {{w0[0], w0[1]}, {w0[2], w0[3]}, {w1[0], w1[1]}, {w1[2], w1[3]}, {w2[0], w2[1]}, {w2[2], w2[3]}, {w3[0], w3[1]}, {w3[2], w3[3]}};
; #pragma unroll
;                 for (int q = 0; q < 4; ++q) { const float h = xx[q][j][i]; const r_f32x2 hh = {h, h};
; #pragma unroll
;                     for (int e = 0; e < 8; ++e) lg2[q][e] = __builtin_elementwise_fma(hh, wv[e], lg2[q][e]); }
	v_pk_fma_f32 v[16:17], v[2:3], v[12:13], v[6:7]
	v_pk_fma_f32 v[14:15], v[4:5], v[14:15], v[8:9]
	v_med3_f32 v2, v16, s33, v226
	v_med3_f32 v3, v17, s33, v226
	v_cvt_pk_fp8_f32 v94, v2, v3
	v_med3_f32 v2, v14, s33, v226
	v_med3_f32 v3, v15, s33, v226
	v_pk_mul_f32 v[4:5], v[96:97], v[112:113] op_sel_hi:[1,0]
	v_cvt_pk_fp8_f32 v94, v2, v3 op_sel:[0,0,1]
	v_pk_mul_f32 v[2:3], v[10:11], v[112:113] op_sel_hi:[1,0]
	s_waitcnt lgkmcnt(0)
	v_pk_fma_f32 v[10:11], v[88:89], v[4:5], v[92:93]
	v_pk_fma_f32 v[12:13], v[86:87], v[2:3], v[90:91]
	v_pk_mul_f32 v[6:7], v[104:105], v[112:113] op_sel_hi:[1,0]
	v_med3_f32 v2, v12, s33, v226
	v_med3_f32 v3, v13, s33, v226
	v_cvt_pk_fp8_f32 v95, v2, v3
	v_med3_f32 v2, v10, s33, v226
	v_med3_f32 v3, v11, s33, v226
	v_mov_b32_e32 v96, v183
	v_cvt_pk_fp8_f32 v95, v2, v3 op_sel:[0,0,1]
	ds_read_b128 v[2:5], v99 offset:6144
	ds_read_b128 v[86:89], v99 offset:10240
	v_cvt_pk_bf16_f32 v83, v102, v103
	v_pk_mul_f32 v[104:105], v[102:103], v[112:113] op_sel_hi:[1,0]
	ds_read_b128 v[90:93], v99 offset:7168
	ds_read_b128 v[100:103], v99 offset:11264
	v_mov_b32_e32 v97, v183
	s_waitcnt lgkmcnt(2)
	v_pk_fma_f32 v[8:9], v[6:7], v[2:3], v[86:87]
	v_pk_fma_f32 v[6:7], v[104:105], v[4:5], v[88:89]
	v_med3_f32 v2, v8, s33, v226
	v_med3_f32 v3, v9, s33, v226
	v_cvt_pk_fp8_f32 v96, v2, v3
	v_med3_f32 v2, v6, s33, v226
	v_med3_f32 v3, v7, s33, v226
	v_pk_mul_f32 v[86:87], v[106:107], v[112:113] op_sel_hi:[1,0]
	v_cvt_pk_fp8_f32 v96, v2, v3 op_sel:[0,0,1]
	v_pk_mul_f32 v[2:3], v[108:109], v[112:113] op_sel_hi:[1,0]
	v_cvt_pk_bf16_f32 v84, v108, v109
	s_waitcnt lgkmcnt(0)
	v_pk_fma_f32 v[4:5], v[2:3], v[90:91], v[100:101]
	v_cvt_pk_bf16_f32 v85, v106, v107
	v_med3_f32 v2, v4, s33, v226
	v_med3_f32 v3, v5, s33, v226
	v_cvt_pk_fp8_f32 v97, v2, v3
	v_pk_fma_f32 v[2:3], v[86:87], v[92:93], v[102:103]
	global_store_dwordx4 v[110:111], v[82:85], off offset:16
	v_med3_f32 v86, v2, s33, v226
	v_med3_f32 v87, v3, s33, v226
	v_cvt_pk_fp8_f32 v97, v86, v87 op_sel:[0,0,1]
	v_lshl_add_u64 v[86:87], v[40:41], 0, s[40:41]
	ds_read_b128 v[82:85], v1
	s_mov_b32 s2, 0xc2ce8ed0
	global_store_dwordx4 v[86:87], v[94:97], off
	ds_read_b128 v[86:89], v1 offset:16
	ds_read_b128 v[90:93], v1 offset:32
	ds_read_b128 v[94:97], v1 offset:48
	s_waitcnt lgkmcnt(3)
	v_pk_fma_f32 v[100:101], v[66:67], v[82:83], 0 op_sel_hi:[0,1,0]
	v_pk_fma_f32 v[102:103], v[66:67], v[84:85], 0 op_sel_hi:[0,1,0]
	s_waitcnt lgkmcnt(2)
	v_pk_fma_f32 v[104:105], v[66:67], v[86:87], 0 op_sel_hi:[0,1,0]
	v_pk_fma_f32 v[106:107], v[66:67], v[88:89], 0 op_sel_hi:[0,1,0]
	s_waitcnt lgkmcnt(1)
	v_pk_fma_f32 v[108:109], v[66:67], v[90:91], 0 op_sel_hi:[0,1,0]
	v_pk_fma_f32 v[110:111], v[66:67], v[92:93], 0 op_sel_hi:[0,1,0]
	s_waitcnt lgkmcnt(0)
	v_pk_fma_f32 v[112:113], v[66:67], v[94:95], 0 op_sel_hi:[0,1,0]
	v_pk_fma_f32 v[114:115], v[66:67], v[96:97], 0 op_sel_hi:[0,1,0]
	v_pk_fma_f32 v[116:117], v[74:75], v[82:83], 0 op_sel_hi:[0,1,0]
	v_pk_fma_f32 v[118:119], v[74:75], v[84:85], 0 op_sel_hi:[0,1,0]
	v_pk_fma_f32 v[120:121], v[74:75], v[86:87], 0 op_sel_hi:[0,1,0]
	v_pk_fma_f32 v[122:123], v[74:75], v[88:89], 0 op_sel_hi:[0,1,0]
	v_pk_fma_f32 v[124:125], v[74:75], v[90:91], 0 op_sel_hi:[0,1,0]
	v_pk_fma_f32 v[126:127], v[74:75], v[92:93], 0 op_sel_hi:[0,1,0]
	v_pk_fma_f32 v[128:129], v[74:75], v[94:95], 0 op_sel_hi:[0,1,0]
	v_pk_fma_f32 v[130:131], v[74:75], v[96:97], 0 op_sel_hi:[0,1,0]
	v_pk_fma_f32 v[132:133], v[80:81], v[82:83], 0 op_sel_hi:[0,1,0]
	v_pk_fma_f32 v[134:135], v[80:81], v[84:85], 0 op_sel_hi:[0,1,0]
	v_pk_fma_f32 v[136:137], v[80:81], v[86:87], 0 op_sel_hi:[0,1,0]
	v_pk_fma_f32 v[138:139], v[80:81], v[88:89], 0 op_sel_hi:[0,1,0]
	v_pk_fma_f32 v[140:141], v[80:81], v[90:91], 0 op_sel_hi:[0,1,0]
	v_pk_fma_f32 v[142:143], v[80:81], v[92:93], 0 op_sel_hi:[0,1,0]
	v_pk_fma_f32 v[144:145], v[80:81], v[94:95], 0 op_sel_hi:[0,1,0]
	v_pk_fma_f32 v[146:147], v[80:81], v[96:97], 0 op_sel_hi:[0,1,0]
	v_pk_fma_f32 v[148:149], v[16:17], v[82:83], 0 op_sel_hi:[0,1,0]
	v_pk_fma_f32 v[150:151], v[16:17], v[84:85], 0 op_sel_hi:[0,1,0]
	v_pk_fma_f32 v[152:153], v[16:17], v[86:87], 0 op_sel_hi:[0,1,0]
	v_pk_fma_f32 v[154:155], v[16:17], v[88:89], 0 op_sel_hi:[0,1,0]
	v_pk_fma_f32 v[156:157], v[16:17], v[90:91], 0 op_sel_hi:[0,1,0]
	v_pk_fma_f32 v[158:159], v[16:17], v[92:93], 0 op_sel_hi:[0,1,0]
	v_pk_fma_f32 v[160:161], v[16:17], v[94:95], 0 op_sel_hi:[0,1,0]
	v_pk_fma_f32 v[162:163], v[16:17], v[96:97], 0 op_sel_hi:[0,1,0]
	ds_read_b128 v[82:85], v1 offset:64
	ds_read_b128 v[86:89], v1 offset:80
	ds_read_b128 v[90:93], v1 offset:96
	ds_read_b128 v[94:97], v1 offset:112
	s_waitcnt lgkmcnt(3)
	v_pk_fma_f32 v[100:101], v[66:67], v[82:83], v[100:101] op_sel:[1,0,0]
	v_pk_fma_f32 v[102:103], v[66:67], v[84:85], v[102:103] op_sel:[1,0,0]
	s_waitcnt lgkmcnt(2)
	v_pk_fma_f32 v[104:105], v[66:67], v[86:87], v[104:105] op_sel:[1,0,0]
	v_pk_fma_f32 v[106:107], v[66:67], v[88:89], v[106:107] op_sel:[1,0,0]
	s_waitcnt lgkmcnt(1)
	v_pk_fma_f32 v[108:109], v[66:67], v[90:91], v[108:109] op_sel:[1,0,0]
	v_pk_fma_f32 v[110:111], v[66:67], v[92:93], v[110:111] op_sel:[1,0,0]
	s_waitcnt lgkmcnt(0)
; #define LAS __attribute__((address_space(3)))
; __device__ __forceinline__ void phase_post_mix(Frame& F, int l) {
;     ...
;         for (int j = 0; j < 4; ++j) { const LAS float* wg = rws + (lane + 64 * j) * 68;
; #pragma unroll
;             for (int i = 0; i < 4; ++i) { const f32x4 w0 = *(const LAS f32x4*)(wg + 16 * i), w1 = *(const LAS f32x4*)(wg + 16 * i + 4), w2 = *(const LAS f32x4*)(wg + 16 * i + 8), w3 = *(const LAS f32x4*)(wg + 16 * i + 12);
;                 const r_f32x2 wv[8] = {{w0[0], w0[1]}, {w0[2], w0[3]}, {w1[0], w1[1]}, {w1[2], w1[3]}, {w2[0], w2[1]}, {w2[2], w2[3]}, {w3[0], w3[1]}, {w3[2], w3[3]}};
; #pragma unroll
;                 for (int q = 0; q < 4; ++q) { const float h = xx[q][j][i]; const r_f32x2 hh = {h, h};
; #pragma unroll
;                     for (int e = 0; e < 8; ++e) lg2[q][e] = __builtin_elementwise_fma(hh, wv[e], lg2[q][e]); }
; #pragma unroll
;                 for (int q = 0; q < 4; ++q)
;                     asm volatile("" : "+v"(lg2[q][0]), "+v"(lg2[q][1]), "+v"(lg2[q][2]), "+v"(lg2[q][3]), "+v"(lg2[q][4]), "+v"(lg2[q][5]), "+v"(lg2[q][6]), "+v"(lg2[q][7]));
;                 } }
	v_pk_fma_f32 v[112:113], v[66:67], v[94:95], v[112:113] op_sel:[1,0,0]
	v_pk_fma_f32 v[66:67], v[66:67], v[96:97], v[114:115] op_sel:[1,0,0]
	v_pk_fma_f32 v[114:115], v[74:75], v[82:83], v[116:117] op_sel:[1,0,0]
	v_pk_fma_f32 v[116:117], v[74:75], v[84:85], v[118:119] op_sel:[1,0,0]
	v_pk_fma_f32 v[118:119], v[74:75], v[86:87], v[120:121] op_sel:[1,0,0]
	v_pk_fma_f32 v[120:121], v[74:75], v[88:89], v[122:123] op_sel:[1,0,0]
	v_pk_fma_f32 v[122:123], v[74:75], v[90:91], v[124:125] op_sel:[1,0,0]
	v_pk_fma_f32 v[124:125], v[74:75], v[92:93], v[126:127] op_sel:[1,0,0]
	v_pk_fma_f32 v[126:127], v[74:75], v[94:95], v[128:129] op_sel:[1,0,0]
	v_pk_fma_f32 v[74:75], v[74:75], v[96:97], v[130:131] op_sel:[1,0,0]
	v_pk_fma_f32 v[128:129], v[80:81], v[82:83], v[132:133] op_sel:[1,0,0]
	v_pk_fma_f32 v[130:131], v[80:81], v[84:85], v[134:135] op_sel:[1,0,0]
	v_pk_fma_f32 v[132:133], v[80:81], v[86:87], v[136:137] op_sel:[1,0,0]
	v_pk_fma_f32 v[134:135], v[80:81], v[88:89], v[138:139] op_sel:[1,0,0]
	v_pk_fma_f32 v[136:137], v[80:81], v[90:91], v[140:141] op_sel:[1,0,0]
	v_pk_fma_f32 v[138:139], v[80:81], v[92:93], v[142:143] op_sel:[1,0,0]
	v_pk_fma_f32 v[140:141], v[80:81], v[94:95], v[144:145] op_sel:[1,0,0]
	v_pk_fma_f32 v[142:143], v[80:81], v[96:97], v[146:147] op_sel:[1,0,0]
	v_pk_fma_f32 v[144:145], v[16:17], v[82:83], v[148:149] op_sel:[1,0,0]
	v_pk_fma_f32 v[146:147], v[16:17], v[84:85], v[150:151] op_sel:[1,0,0]
	v_pk_fma_f32 v[148:149], v[16:17], v[86:87], v[152:153] op_sel:[1,0,0]
	v_pk_fma_f32 v[150:151], v[16:17], v[88:89], v[154:155] op_sel:[1,0,0]
	v_pk_fma_f32 v[152:153], v[16:17], v[90:91], v[156:157] op_sel:[1,0,0]
	v_pk_fma_f32 v[154:155], v[16:17], v[92:93], v[158:159] op_sel:[1,0,0]
	v_pk_fma_f32 v[156:157], v[16:17], v[94:95], v[160:161] op_sel:[1,0,0]
	v_pk_fma_f32 v[16:17], v[16:17], v[96:97], v[162:163] op_sel:[1,0,0]
	s_nop 0
	ds_read_b128 v[80:83], v1 offset:128
	ds_read_b128 v[84:87], v1 offset:144
	ds_read_b128 v[88:91], v1 offset:160
	ds_read_b128 v[92:95], v1 offset:176
	s_waitcnt lgkmcnt(3)
	v_pk_fma_f32 v[96:97], v[60:61], v[80:81], v[100:101] op_sel_hi:[0,1,1]
	v_pk_fma_f32 v[100:101], v[60:61], v[82:83], v[102:103] op_sel_hi:[0,1,1]
	s_waitcnt lgkmcnt(2)
	v_pk_fma_f32 v[102:103], v[60:61], v[84:85], v[104:105] op_sel_hi:[0,1,1]
	v_pk_fma_f32 v[104:105], v[60:61], v[86:87], v[106:107] op_sel_hi:[0,1,1]
	s_waitcnt lgkmcnt(1)
	v_pk_fma_f32 v[106:107], v[60:61], v[88:89], v[108:109] op_sel_hi:[0,1,1]
	v_pk_fma_f32 v[108:109], v[60:61], v[90:91], v[110:111] op_sel_hi:[0,1,1]
	s_waitcnt lgkmcnt(0)
	v_pk_fma_f32 v[110:111], v[60:61], v[92:93], v[112:113] op_sel_hi:[0,1,1]
	v_pk_fma_f32 v[66:67], v[60:61], v[94:95], v[66:67] op_sel_hi:[0,1,1]
	v_pk_fma_f32 v[112:113], v[70:71], v[80:81], v[114:115] op_sel_hi:[0,1,1]
	v_pk_fma_f32 v[114:115], v[70:71], v[82:83], v[116:117] op_sel_hi:[0,1,1]
	v_pk_fma_f32 v[116:117], v[70:71], v[84:85], v[118:119] op_sel_hi:[0,1,1]
	v_pk_fma_f32 v[118:119], v[70:71], v[86:87], v[120:121] op_sel_hi:[0,1,1]
	v_pk_fma_f32 v[120:121], v[70:71], v[88:89], v[122:123] op_sel_hi:[0,1,1]
	v_pk_fma_f32 v[122:123], v[70:71], v[90:91], v[124:125] op_sel_hi:[0,1,1]
	v_pk_fma_f32 v[124:125], v[70:71], v[92:93], v[126:127] op_sel_hi:[0,1,1]
	v_pk_fma_f32 v[74:75], v[70:71], v[94:95], v[74:75] op_sel_hi:[0,1,1]
	v_pk_fma_f32 v[126:127], v[78:79], v[80:81], v[128:129] op_sel_hi:[0,1,1]
	v_pk_fma_f32 v[128:129], v[78:79], v[82:83], v[130:131] op_sel_hi:[0,1,1]
	v_pk_fma_f32 v[130:131], v[78:79], v[84:85], v[132:133] op_sel_hi:[0,1,1]
	v_pk_fma_f32 v[132:133], v[78:79], v[86:87], v[134:135] op_sel_hi:[0,1,1]
	v_pk_fma_f32 v[134:135], v[78:79], v[88:89], v[136:137] op_sel_hi:[0,1,1]
	v_pk_fma_f32 v[136:137], v[78:79], v[90:91], v[138:139] op_sel_hi:[0,1,1]
	v_pk_fma_f32 v[138:139], v[78:79], v[92:93], v[140:141] op_sel_hi:[0,1,1]
	v_pk_fma_f32 v[140:141], v[78:79], v[94:95], v[142:143] op_sel_hi:[0,1,1]
	v_pk_fma_f32 v[142:143], v[14:15], v[80:81], v[144:145] op_sel_hi:[0,1,1]
	v_pk_fma_f32 v[144:145], v[14:15], v[82:83], v[146:147] op_sel_hi:[0,1,1]
	v_pk_fma_f32 v[146:147], v[14:15], v[84:85], v[148:149] op_sel_hi:[0,1,1]
	v_pk_fma_f32 v[148:149], v[14:15], v[86:87], v[150:151] op_sel_hi:[0,1,1]
	v_pk_fma_f32 v[150:151], v[14:15], v[88:89], v[152:153] op_sel_hi:[0,1,1]
	v_pk_fma_f32 v[152:153], v[14:15], v[90:91], v[154:155] op_sel_hi:[0,1,1]
	v_pk_fma_f32 v[154:155], v[14:15], v[92:93], v[156:157] op_sel_hi:[0,1,1]
	v_pk_fma_f32 v[16:17], v[14:15], v[94:95], v[16:17] op_sel_hi:[0,1,1]
	ds_read_b128 v[80:83], v1 offset:192
	ds_read_b128 v[84:87], v1 offset:208
	ds_read_b128 v[88:91], v1 offset:224
	ds_read_b128 v[92:95], v1 offset:240
	s_waitcnt lgkmcnt(3)
	v_pk_fma_f32 v[96:97], v[60:61], v[80:81], v[96:97] op_sel:[1,0,0]
	v_pk_fma_f32 v[100:101], v[60:61], v[82:83], v[100:101] op_sel:[1,0,0]
	s_waitcnt lgkmcnt(2)
	v_pk_fma_f32 v[102:103], v[60:61], v[84:85], v[102:103] op_sel:[1,0,0]
	v_pk_fma_f32 v[104:105], v[60:61], v[86:87], v[104:105] op_sel:[1,0,0]
	s_waitcnt lgkmcnt(1)
	v_pk_fma_f32 v[106:107], v[60:61], v[88:89], v[106:107] op_sel:[1,0,0]
	v_pk_fma_f32 v[108:109], v[60:61], v[90:91], v[108:109] op_sel:[1,0,0]
	s_waitcnt lgkmcnt(0)
; #define LAS __attribute__((address_space(3)))
; __device__ __forceinline__ void phase_post_mix(Frame& F, int l) {
;     ...
;         for (int j = 0; j < 4; ++j) { const LAS float* wg = rws + (lane + 64 * j) * 68;
; #pragma unroll
;             for (int i = 0; i < 4; ++i) { const f32x4 w0 = *(const LAS f32x4*)(wg + 16 * i), w1 = *(const LAS f32x4*)(wg + 16 * i + 4), w2 = *(const LAS f32x4*)(wg + 16 * i + 8), w3 = *(const LAS f32x4*)(wg + 16 * i + 12);
;                 const r_f32x2 wv[8] = {{w0[0], w0[1]}, {w0[2], w0[3]}, {w1[0], w1[1]}, {w1[2], w1[3]}, {w2[0], w2[1]}, {w2[2], w2[3]}, {w3[0], w3[1]}, {w3[2], w3[3]}};
; #pragma unroll
;                 for (int q = 0; q < 4; ++q) { const float h = xx[q][j][i]; const r_f32x2 hh = {h, h};
; #pragma unroll
;                     for (int e = 0; e < 8; ++e) lg2[q][e] = __builtin_elementwise_fma(hh, wv[e], lg2[q][e]); }
; #pragma unroll
;                 for (int q = 0; q < 4; ++q)
;                     asm volatile("" : "+v"(lg2[q][0]), "+v"(lg2[q][1]), "+v"(lg2[q][2]), "+v"(lg2[q][3]), "+v"(lg2[q][4]), "+v"(lg2[q][5]), "+v"(lg2[q][6]), "+v"(lg2[q][7]));
;                 } }
	v_pk_fma_f32 v[110:111], v[60:61], v[92:93], v[110:111] op_sel:[1,0,0]
	v_pk_fma_f32 v[60:61], v[60:61], v[94:95], v[66:67] op_sel:[1,0,0]
	v_pk_fma_f32 v[66:67], v[70:71], v[80:81], v[112:113] op_sel:[1,0,0]
	v_pk_fma_f32 v[112:113], v[70:71], v[82:83], v[114:115] op_sel:[1,0,0]
	v_pk_fma_f32 v[114:115], v[70:71], v[84:85], v[116:117] op_sel:[1,0,0]
	v_pk_fma_f32 v[116:117], v[70:71], v[86:87], v[118:119] op_sel:[1,0,0]
	v_pk_fma_f32 v[118:119], v[70:71], v[88:89], v[120:121] op_sel:[1,0,0]
	v_pk_fma_f32 v[120:121], v[70:71], v[90:91], v[122:123] op_sel:[1,0,0]
	v_pk_fma_f32 v[122:123], v[70:71], v[92:93], v[124:125] op_sel:[1,0,0]
	v_pk_fma_f32 v[70:71], v[70:71], v[94:95], v[74:75] op_sel:[1,0,0]
	v_pk_fma_f32 v[74:75], v[78:79], v[80:81], v[126:127] op_sel:[1,0,0]
	v_pk_fma_f32 v[124:125], v[78:79], v[82:83], v[128:129] op_sel:[1,0,0]
	v_pk_fma_f32 v[126:127], v[78:79], v[84:85], v[130:131] op_sel:[1,0,0]
	v_pk_fma_f32 v[128:129], v[78:79], v[86:87], v[132:133] op_sel:[1,0,0]
	v_pk_fma_f32 v[130:131], v[78:79], v[88:89], v[134:135] op_sel:[1,0,0]
	v_pk_fma_f32 v[132:133], v[78:79], v[90:91], v[136:137] op_sel:[1,0,0]
	v_pk_fma_f32 v[134:135], v[78:79], v[92:93], v[138:139] op_sel:[1,0,0]
	v_pk_fma_f32 v[136:137], v[78:79], v[94:95], v[140:141] op_sel:[1,0,0]
	v_pk_fma_f32 v[138:139], v[14:15], v[80:81], v[142:143] op_sel:[1,0,0]
	v_pk_fma_f32 v[140:141], v[14:15], v[82:83], v[144:145] op_sel:[1,0,0]
	v_pk_fma_f32 v[142:143], v[14:15], v[84:85], v[146:147] op_sel:[1,0,0]
	v_pk_fma_f32 v[144:145], v[14:15], v[86:87], v[148:149] op_sel:[1,0,0]
	v_pk_fma_f32 v[146:147], v[14:15], v[88:89], v[150:151] op_sel:[1,0,0]
	v_pk_fma_f32 v[90:91], v[14:15], v[90:91], v[152:153] op_sel:[1,0,0]
	v_pk_fma_f32 v[92:93], v[14:15], v[92:93], v[154:155] op_sel:[1,0,0]
	v_pk_fma_f32 v[94:95], v[14:15], v[94:95], v[16:17] op_sel:[1,0,0]
	s_nop 0
	ds_read_b128 v[14:17], v1 offset:17408
	ds_read_b128 v[78:81], v1 offset:17424
	ds_read_b128 v[82:85], v1 offset:17440
	ds_read_b128 v[86:89], v1 offset:17456
	s_waitcnt lgkmcnt(3)
	v_pk_fma_f32 v[96:97], v[54:55], v[14:15], v[96:97] op_sel_hi:[0,1,1]
	v_pk_fma_f32 v[100:101], v[54:55], v[16:17], v[100:101] op_sel_hi:[0,1,1]
	s_waitcnt lgkmcnt(2)
	v_pk_fma_f32 v[102:103], v[54:55], v[78:79], v[102:103] op_sel_hi:[0,1,1]
	v_pk_fma_f32 v[104:105], v[54:55], v[80:81], v[104:105] op_sel_hi:[0,1,1]
	s_waitcnt lgkmcnt(1)
	v_pk_fma_f32 v[106:107], v[54:55], v[82:83], v[106:107] op_sel_hi:[0,1,1]
	v_pk_fma_f32 v[108:109], v[54:55], v[84:85], v[108:109] op_sel_hi:[0,1,1]
	s_waitcnt lgkmcnt(0)
	v_pk_fma_f32 v[110:111], v[54:55], v[86:87], v[110:111] op_sel_hi:[0,1,1]
	v_pk_fma_f32 v[60:61], v[54:55], v[88:89], v[60:61] op_sel_hi:[0,1,1]
	v_pk_fma_f32 v[66:67], v[64:65], v[14:15], v[66:67] op_sel_hi:[0,1,1]
	v_pk_fma_f32 v[112:113], v[64:65], v[16:17], v[112:113] op_sel_hi:[0,1,1]
	v_pk_fma_f32 v[114:115], v[64:65], v[78:79], v[114:115] op_sel_hi:[0,1,1]
	v_pk_fma_f32 v[116:117], v[64:65], v[80:81], v[116:117] op_sel_hi:[0,1,1]
	v_pk_fma_f32 v[118:119], v[64:65], v[82:83], v[118:119] op_sel_hi:[0,1,1]
	v_pk_fma_f32 v[120:121], v[64:65], v[84:85], v[120:121] op_sel_hi:[0,1,1]
	v_pk_fma_f32 v[122:123], v[64:65], v[86:87], v[122:123] op_sel_hi:[0,1,1]
	v_pk_fma_f32 v[70:71], v[64:65], v[88:89], v[70:71] op_sel_hi:[0,1,1]
	v_pk_fma_f32 v[74:75], v[76:77], v[14:15], v[74:75] op_sel_hi:[0,1,1]
	v_pk_fma_f32 v[124:125], v[76:77], v[16:17], v[124:125] op_sel_hi:[0,1,1]
	v_pk_fma_f32 v[126:127], v[76:77], v[78:79], v[126:127] op_sel_hi:[0,1,1]
	v_pk_fma_f32 v[128:129], v[76:77], v[80:81], v[128:129] op_sel_hi:[0,1,1]
	v_pk_fma_f32 v[130:131], v[76:77], v[82:83], v[130:131] op_sel_hi:[0,1,1]
	v_pk_fma_f32 v[132:133], v[76:77], v[84:85], v[132:133] op_sel_hi:[0,1,1]
	v_pk_fma_f32 v[134:135], v[76:77], v[86:87], v[134:135] op_sel_hi:[0,1,1]
	v_pk_fma_f32 v[136:137], v[76:77], v[88:89], v[136:137] op_sel_hi:[0,1,1]
	v_pk_fma_f32 v[138:139], v[12:13], v[14:15], v[138:139] op_sel_hi:[0,1,1]
	v_pk_fma_f32 v[140:141], v[12:13], v[16:17], v[140:141] op_sel_hi:[0,1,1]
	v_pk_fma_f32 v[142:143], v[12:13], v[78:79], v[142:143] op_sel_hi:[0,1,1]
	v_pk_fma_f32 v[144:145], v[12:13], v[80:81], v[144:145] op_sel_hi:[0,1,1]
	v_pk_fma_f32 v[146:147], v[12:13], v[82:83], v[146:147] op_sel_hi:[0,1,1]
	v_pk_fma_f32 v[90:91], v[12:13], v[84:85], v[90:91] op_sel_hi:[0,1,1]
	v_pk_fma_f32 v[92:93], v[12:13], v[86:87], v[92:93] op_sel_hi:[0,1,1]
	v_pk_fma_f32 v[94:95], v[12:13], v[88:89], v[94:95] op_sel_hi:[0,1,1]
	ds_read_b128 v[14:17], v1 offset:17472
	ds_read_b128 v[78:81], v1 offset:17488
	ds_read_b128 v[82:85], v1 offset:17504
	ds_read_b128 v[86:89], v1 offset:17520
	s_waitcnt lgkmcnt(3)
	v_pk_fma_f32 v[96:97], v[54:55], v[14:15], v[96:97] op_sel:[1,0,0]
	v_pk_fma_f32 v[100:101], v[54:55], v[16:17], v[100:101] op_sel:[1,0,0]
	s_waitcnt lgkmcnt(2)
	v_pk_fma_f32 v[102:103], v[54:55], v[78:79], v[102:103] op_sel:[1,0,0]
	v_pk_fma_f32 v[104:105], v[54:55], v[80:81], v[104:105] op_sel:[1,0,0]
	s_waitcnt lgkmcnt(1)
	v_pk_fma_f32 v[106:107], v[54:55], v[82:83], v[106:107] op_sel:[1,0,0]
	v_pk_fma_f32 v[108:109], v[54:55], v[84:85], v[108:109] op_sel:[1,0,0]
	s_waitcnt lgkmcnt(0)
; #define LAS __attribute__((address_space(3)))
; __device__ __forceinline__ void phase_post_mix(Frame& F, int l) {
;     ...
;         for (int j = 0; j < 4; ++j) { const LAS float* wg = rws + (lane + 64 * j) * 68;
; #pragma unroll
;             for (int i = 0; i < 4; ++i) { const f32x4 w0 = *(const LAS f32x4*)(wg + 16 * i), w1 = *(const LAS f32x4*)(wg + 16 * i + 4), w2 = *(const LAS f32x4*)(wg + 16 * i + 8), w3 = *(const LAS f32x4*)(wg + 16 * i + 12);
;                 const r_f32x2 wv[8] = {{w0[0], w0[1]}, {w0[2], w0[3]}, {w1[0], w1[1]}, {w1[2], w1[3]}, {w2[0], w2[1]}, {w2[2], w2[3]}, {w3[0], w3[1]}, {w3[2], w3[3]}};
; #pragma unroll
;                 for (int q = 0; q < 4; ++q) { const float h = xx[q][j][i]; const r_f32x2 hh = {h, h};
; #pragma unroll
;                     for (int e = 0; e < 8; ++e) lg2[q][e] = __builtin_elementwise_fma(hh, wv[e], lg2[q][e]); }
; #pragma unroll
;                 for (int q = 0; q < 4; ++q)
;                     asm volatile("" : "+v"(lg2[q][0]), "+v"(lg2[q][1]), "+v"(lg2[q][2]), "+v"(lg2[q][3]), "+v"(lg2[q][4]), "+v"(lg2[q][5]), "+v"(lg2[q][6]), "+v"(lg2[q][7]));
;                 } }
	v_pk_fma_f32 v[110:111], v[54:55], v[86:87], v[110:111] op_sel:[1,0,0]
	v_pk_fma_f32 v[54:55], v[54:55], v[88:89], v[60:61] op_sel:[1,0,0]
	v_pk_fma_f32 v[60:61], v[64:65], v[14:15], v[66:67] op_sel:[1,0,0]
	v_pk_fma_f32 v[112:113], v[64:65], v[16:17], v[112:113] op_sel:[1,0,0]
	v_pk_fma_f32 v[114:115], v[64:65], v[78:79], v[114:115] op_sel:[1,0,0]
	v_pk_fma_f32 v[116:117], v[64:65], v[80:81], v[116:117] op_sel:[1,0,0]
	v_pk_fma_f32 v[118:119], v[64:65], v[82:83], v[118:119] op_sel:[1,0,0]
	v_pk_fma_f32 v[120:121], v[64:65], v[84:85], v[120:121] op_sel:[1,0,0]
	v_pk_fma_f32 v[122:123], v[64:65], v[86:87], v[122:123] op_sel:[1,0,0]
	v_pk_fma_f32 v[70:71], v[64:65], v[88:89], v[70:71] op_sel:[1,0,0]
	v_pk_fma_f32 v[148:149], v[76:77], v[14:15], v[74:75] op_sel:[1,0,0]
	v_pk_fma_f32 v[124:125], v[76:77], v[16:17], v[124:125] op_sel:[1,0,0]
	v_pk_fma_f32 v[126:127], v[76:77], v[78:79], v[126:127] op_sel:[1,0,0]
	v_pk_fma_f32 v[128:129], v[76:77], v[80:81], v[128:129] op_sel:[1,0,0]
	v_pk_fma_f32 v[130:131], v[76:77], v[82:83], v[130:131] op_sel:[1,0,0]
	v_pk_fma_f32 v[132:133], v[76:77], v[84:85], v[132:133] op_sel:[1,0,0]
	v_pk_fma_f32 v[134:135], v[76:77], v[86:87], v[134:135] op_sel:[1,0,0]
	v_pk_fma_f32 v[136:137], v[76:77], v[88:89], v[136:137] op_sel:[1,0,0]
	v_pk_fma_f32 v[138:139], v[12:13], v[14:15], v[138:139] op_sel:[1,0,0]
	v_pk_fma_f32 v[16:17], v[12:13], v[16:17], v[140:141] op_sel:[1,0,0]
	v_pk_fma_f32 v[140:141], v[12:13], v[78:79], v[142:143] op_sel:[1,0,0]
	v_pk_fma_f32 v[142:143], v[12:13], v[80:81], v[144:145] op_sel:[1,0,0]
	v_pk_fma_f32 v[82:83], v[12:13], v[82:83], v[146:147] op_sel:[1,0,0]
	v_pk_fma_f32 v[84:85], v[12:13], v[84:85], v[90:91] op_sel:[1,0,0]
	v_pk_fma_f32 v[86:87], v[12:13], v[86:87], v[92:93] op_sel:[1,0,0]
	v_pk_fma_f32 v[88:89], v[12:13], v[88:89], v[94:95] op_sel:[1,0,0]
	s_nop 0
	ds_read_b128 v[12:15], v1 offset:17536
	ds_read_b128 v[64:67], v1 offset:17552
	ds_read_b128 v[74:77], v1 offset:17568
	ds_read_b128 v[78:81], v1 offset:17584
	s_waitcnt lgkmcnt(3)
	v_pk_fma_f32 v[90:91], v[32:33], v[12:13], v[96:97] op_sel_hi:[0,1,1]
	v_pk_fma_f32 v[92:93], v[32:33], v[14:15], v[100:101] op_sel_hi:[0,1,1]
	s_waitcnt lgkmcnt(2)
	v_pk_fma_f32 v[94:95], v[32:33], v[64:65], v[102:103] op_sel_hi:[0,1,1]
	v_pk_fma_f32 v[96:97], v[32:33], v[66:67], v[104:105] op_sel_hi:[0,1,1]
	s_waitcnt lgkmcnt(1)
	v_pk_fma_f32 v[100:101], v[32:33], v[74:75], v[106:107] op_sel_hi:[0,1,1]
	v_pk_fma_f32 v[102:103], v[32:33], v[76:77], v[108:109] op_sel_hi:[0,1,1]
	s_waitcnt lgkmcnt(0)
	v_pk_fma_f32 v[104:105], v[32:33], v[78:79], v[110:111] op_sel_hi:[0,1,1]
	v_pk_fma_f32 v[54:55], v[32:33], v[80:81], v[54:55] op_sel_hi:[0,1,1]
	v_pk_fma_f32 v[60:61], v[58:59], v[12:13], v[60:61] op_sel_hi:[0,1,1]
	v_pk_fma_f32 v[106:107], v[58:59], v[14:15], v[112:113] op_sel_hi:[0,1,1]
	v_pk_fma_f32 v[108:109], v[58:59], v[64:65], v[114:115] op_sel_hi:[0,1,1]
	v_pk_fma_f32 v[110:111], v[58:59], v[66:67], v[116:117] op_sel_hi:[0,1,1]
	v_pk_fma_f32 v[112:113], v[58:59], v[74:75], v[118:119] op_sel_hi:[0,1,1]
	v_pk_fma_f32 v[114:115], v[58:59], v[76:77], v[120:121] op_sel_hi:[0,1,1]
	v_pk_fma_f32 v[116:117], v[58:59], v[78:79], v[122:123] op_sel_hi:[0,1,1]
	v_pk_fma_f32 v[70:71], v[58:59], v[80:81], v[70:71] op_sel_hi:[0,1,1]
	v_pk_fma_f32 v[118:119], v[72:73], v[12:13], v[148:149] op_sel_hi:[0,1,1]
	v_pk_fma_f32 v[120:121], v[72:73], v[14:15], v[124:125] op_sel_hi:[0,1,1]
	v_pk_fma_f32 v[122:123], v[72:73], v[64:65], v[126:127] op_sel_hi:[0,1,1]
	v_pk_fma_f32 v[124:125], v[72:73], v[66:67], v[128:129] op_sel_hi:[0,1,1]
	v_pk_fma_f32 v[126:127], v[72:73], v[74:75], v[130:131] op_sel_hi:[0,1,1]
	v_pk_fma_f32 v[128:129], v[72:73], v[76:77], v[132:133] op_sel_hi:[0,1,1]
	v_pk_fma_f32 v[130:131], v[72:73], v[78:79], v[134:135] op_sel_hi:[0,1,1]
	v_pk_fma_f32 v[132:133], v[72:73], v[80:81], v[136:137] op_sel_hi:[0,1,1]
	v_pk_fma_f32 v[134:135], v[10:11], v[12:13], v[138:139] op_sel_hi:[0,1,1]
	v_pk_fma_f32 v[16:17], v[10:11], v[14:15], v[16:17] op_sel_hi:[0,1,1]
	v_pk_fma_f32 v[136:137], v[10:11], v[64:65], v[140:141] op_sel_hi:[0,1,1]
	v_pk_fma_f32 v[138:139], v[10:11], v[66:67], v[142:143] op_sel_hi:[0,1,1]
	v_pk_fma_f32 v[82:83], v[10:11], v[74:75], v[82:83] op_sel_hi:[0,1,1]
	v_pk_fma_f32 v[84:85], v[10:11], v[76:77], v[84:85] op_sel_hi:[0,1,1]
	v_pk_fma_f32 v[86:87], v[10:11], v[78:79], v[86:87] op_sel_hi:[0,1,1]
	v_pk_fma_f32 v[88:89], v[10:11], v[80:81], v[88:89] op_sel_hi:[0,1,1]
	ds_read_b128 v[12:15], v1 offset:17600
	ds_read_b128 v[64:67], v1 offset:17616
	ds_read_b128 v[74:77], v1 offset:17632
	ds_read_b128 v[78:81], v1 offset:17648
	s_waitcnt lgkmcnt(3)
	v_pk_fma_f32 v[90:91], v[32:33], v[12:13], v[90:91] op_sel:[1,0,0]
	v_pk_fma_f32 v[92:93], v[32:33], v[14:15], v[92:93] op_sel:[1,0,0]
	s_waitcnt lgkmcnt(2)
	v_pk_fma_f32 v[94:95], v[32:33], v[64:65], v[94:95] op_sel:[1,0,0]
	v_pk_fma_f32 v[96:97], v[32:33], v[66:67], v[96:97] op_sel:[1,0,0]
	s_waitcnt lgkmcnt(1)
	v_pk_fma_f32 v[100:101], v[32:33], v[74:75], v[100:101] op_sel:[1,0,0]
	v_pk_fma_f32 v[102:103], v[32:33], v[76:77], v[102:103] op_sel:[1,0,0]
	s_waitcnt lgkmcnt(0)
; #define LAS __attribute__((address_space(3)))
; __device__ __forceinline__ void phase_post_mix(Frame& F, int l) {
;     ...
;         for (int j = 0; j < 4; ++j) { const LAS float* wg = rws + (lane + 64 * j) * 68;
; #pragma unroll
;             for (int i = 0; i < 4; ++i) { const f32x4 w0 = *(const LAS f32x4*)(wg + 16 * i), w1 = *(const LAS f32x4*)(wg + 16 * i + 4), w2 = *(const LAS f32x4*)(wg + 16 * i + 8), w3 = *(const LAS f32x4*)(wg + 16 * i + 12);
;                 const r_f32x2 wv[8] = {{w0[0], w0[1]}, {w0[2], w0[3]}, {w1[0], w1[1]}, {w1[2], w1[3]}, {w2[0], w2[1]}, {w2[2], w2[3]}, {w3[0], w3[1]}, {w3[2], w3[3]}};
; #pragma unroll
;                 for (int q = 0; q < 4; ++q) { const float h = xx[q][j][i]; const r_f32x2 hh = {h, h};
; #pragma unroll
;                     for (int e = 0; e < 8; ++e) lg2[q][e] = __builtin_elementwise_fma(hh, wv[e], lg2[q][e]); }
; #pragma unroll
;                 for (int q = 0; q < 4; ++q)
;                     asm volatile("" : "+v"(lg2[q][0]), "+v"(lg2[q][1]), "+v"(lg2[q][2]), "+v"(lg2[q][3]), "+v"(lg2[q][4]), "+v"(lg2[q][5]), "+v"(lg2[q][6]), "+v"(lg2[q][7]));
;                 } }
	v_pk_fma_f32 v[104:105], v[32:33], v[78:79], v[104:105] op_sel:[1,0,0]
	v_pk_fma_f32 v[32:33], v[32:33], v[80:81], v[54:55] op_sel:[1,0,0]
	v_pk_fma_f32 v[54:55], v[58:59], v[12:13], v[60:61] op_sel:[1,0,0]
	v_pk_fma_f32 v[106:107], v[58:59], v[14:15], v[106:107] op_sel:[1,0,0]
	v_pk_fma_f32 v[108:109], v[58:59], v[64:65], v[108:109] op_sel:[1,0,0]
	v_pk_fma_f32 v[110:111], v[58:59], v[66:67], v[110:111] op_sel:[1,0,0]
	v_pk_fma_f32 v[112:113], v[58:59], v[74:75], v[112:113] op_sel:[1,0,0]
	v_pk_fma_f32 v[114:115], v[58:59], v[76:77], v[114:115] op_sel:[1,0,0]
	v_pk_fma_f32 v[116:117], v[58:59], v[78:79], v[116:117] op_sel:[1,0,0]
	v_pk_fma_f32 v[70:71], v[58:59], v[80:81], v[70:71] op_sel:[1,0,0]
	v_pk_fma_f32 v[118:119], v[72:73], v[12:13], v[118:119] op_sel:[1,0,0]
	v_pk_fma_f32 v[120:121], v[72:73], v[14:15], v[120:121] op_sel:[1,0,0]
	v_pk_fma_f32 v[122:123], v[72:73], v[64:65], v[122:123] op_sel:[1,0,0]
	v_pk_fma_f32 v[124:125], v[72:73], v[66:67], v[124:125] op_sel:[1,0,0]
	v_pk_fma_f32 v[126:127], v[72:73], v[74:75], v[126:127] op_sel:[1,0,0]
	v_pk_fma_f32 v[128:129], v[72:73], v[76:77], v[128:129] op_sel:[1,0,0]
	v_pk_fma_f32 v[130:131], v[72:73], v[78:79], v[130:131] op_sel:[1,0,0]
	v_pk_fma_f32 v[72:73], v[72:73], v[80:81], v[132:133] op_sel:[1,0,0]
	v_pk_fma_f32 v[132:133], v[10:11], v[12:13], v[134:135] op_sel:[1,0,0]
	v_pk_fma_f32 v[134:135], v[10:11], v[14:15], v[16:17] op_sel:[1,0,0]
	v_pk_fma_f32 v[136:137], v[10:11], v[64:65], v[136:137] op_sel:[1,0,0]
	v_pk_fma_f32 v[138:139], v[10:11], v[66:67], v[138:139] op_sel:[1,0,0]
	v_pk_fma_f32 v[74:75], v[10:11], v[74:75], v[82:83] op_sel:[1,0,0]
	v_pk_fma_f32 v[76:77], v[10:11], v[76:77], v[84:85] op_sel:[1,0,0]
	v_pk_fma_f32 v[78:79], v[10:11], v[78:79], v[86:87] op_sel:[1,0,0]
	v_pk_fma_f32 v[80:81], v[10:11], v[80:81], v[88:89] op_sel:[1,0,0]
	s_nop 0
	ds_read_b128 v[10:13], v1 offset:34816
	ds_read_b128 v[14:17], v1 offset:34832
	ds_read_b128 v[58:61], v1 offset:34848
	ds_read_b128 v[64:67], v1 offset:34864
	s_waitcnt lgkmcnt(3)
	v_pk_fma_f32 v[82:83], v[28:29], v[10:11], v[90:91] op_sel_hi:[0,1,1]
	v_pk_fma_f32 v[84:85], v[28:29], v[12:13], v[92:93] op_sel_hi:[0,1,1]
	s_waitcnt lgkmcnt(2)
	v_pk_fma_f32 v[86:87], v[28:29], v[14:15], v[94:95] op_sel_hi:[0,1,1]
	v_pk_fma_f32 v[88:89], v[28:29], v[16:17], v[96:97] op_sel_hi:[0,1,1]
	s_waitcnt lgkmcnt(1)
	v_pk_fma_f32 v[90:91], v[28:29], v[58:59], v[100:101] op_sel_hi:[0,1,1]
	v_pk_fma_f32 v[92:93], v[28:29], v[60:61], v[102:103] op_sel_hi:[0,1,1]
	s_waitcnt lgkmcnt(0)
	v_pk_fma_f32 v[94:95], v[28:29], v[64:65], v[104:105] op_sel_hi:[0,1,1]
	v_pk_fma_f32 v[32:33], v[28:29], v[66:67], v[32:33] op_sel_hi:[0,1,1]
	v_pk_fma_f32 v[54:55], v[52:53], v[10:11], v[54:55] op_sel_hi:[0,1,1]
	v_pk_fma_f32 v[96:97], v[52:53], v[12:13], v[106:107] op_sel_hi:[0,1,1]
	v_pk_fma_f32 v[100:101], v[52:53], v[14:15], v[108:109] op_sel_hi:[0,1,1]
	v_pk_fma_f32 v[102:103], v[52:53], v[16:17], v[110:111] op_sel_hi:[0,1,1]
	v_pk_fma_f32 v[104:105], v[52:53], v[58:59], v[112:113] op_sel_hi:[0,1,1]
	v_pk_fma_f32 v[106:107], v[52:53], v[60:61], v[114:115] op_sel_hi:[0,1,1]
	v_pk_fma_f32 v[108:109], v[52:53], v[64:65], v[116:117] op_sel_hi:[0,1,1]
	v_pk_fma_f32 v[70:71], v[52:53], v[66:67], v[70:71] op_sel_hi:[0,1,1]
	v_pk_fma_f32 v[110:111], v[68:69], v[10:11], v[118:119] op_sel_hi:[0,1,1]
	v_pk_fma_f32 v[112:113], v[68:69], v[12:13], v[120:121] op_sel_hi:[0,1,1]
	v_pk_fma_f32 v[114:115], v[68:69], v[14:15], v[122:123] op_sel_hi:[0,1,1]
	v_pk_fma_f32 v[116:117], v[68:69], v[16:17], v[124:125] op_sel_hi:[0,1,1]
	v_pk_fma_f32 v[118:119], v[68:69], v[58:59], v[126:127] op_sel_hi:[0,1,1]
	v_pk_fma_f32 v[120:121], v[68:69], v[60:61], v[128:129] op_sel_hi:[0,1,1]
	v_pk_fma_f32 v[122:123], v[68:69], v[64:65], v[130:131] op_sel_hi:[0,1,1]
	v_pk_fma_f32 v[72:73], v[68:69], v[66:67], v[72:73] op_sel_hi:[0,1,1]
	v_pk_fma_f32 v[124:125], v[8:9], v[10:11], v[132:133] op_sel_hi:[0,1,1]
	v_pk_fma_f32 v[126:127], v[8:9], v[12:13], v[134:135] op_sel_hi:[0,1,1]
	v_pk_fma_f32 v[128:129], v[8:9], v[14:15], v[136:137] op_sel_hi:[0,1,1]
	v_pk_fma_f32 v[130:131], v[8:9], v[16:17], v[138:139] op_sel_hi:[0,1,1]
	v_pk_fma_f32 v[74:75], v[8:9], v[58:59], v[74:75] op_sel_hi:[0,1,1]
	v_pk_fma_f32 v[76:77], v[8:9], v[60:61], v[76:77] op_sel_hi:[0,1,1]
	v_pk_fma_f32 v[78:79], v[8:9], v[64:65], v[78:79] op_sel_hi:[0,1,1]
	v_pk_fma_f32 v[80:81], v[8:9], v[66:67], v[80:81] op_sel_hi:[0,1,1]
	ds_read_b128 v[10:13], v1 offset:34880
	ds_read_b128 v[14:17], v1 offset:34896
	ds_read_b128 v[58:61], v1 offset:34912
	ds_read_b128 v[64:67], v1 offset:34928
	s_waitcnt lgkmcnt(3)
	v_pk_fma_f32 v[82:83], v[28:29], v[10:11], v[82:83] op_sel:[1,0,0]
	v_pk_fma_f32 v[84:85], v[28:29], v[12:13], v[84:85] op_sel:[1,0,0]
	s_waitcnt lgkmcnt(2)
	v_pk_fma_f32 v[86:87], v[28:29], v[14:15], v[86:87] op_sel:[1,0,0]
	v_pk_fma_f32 v[88:89], v[28:29], v[16:17], v[88:89] op_sel:[1,0,0]
	s_waitcnt lgkmcnt(1)
	v_pk_fma_f32 v[90:91], v[28:29], v[58:59], v[90:91] op_sel:[1,0,0]
	v_pk_fma_f32 v[92:93], v[28:29], v[60:61], v[92:93] op_sel:[1,0,0]
	s_waitcnt lgkmcnt(0)
; #define LAS __attribute__((address_space(3)))
; __device__ __forceinline__ void phase_post_mix(Frame& F, int l) {
;     ...
;         for (int j = 0; j < 4; ++j) { const LAS float* wg = rws + (lane + 64 * j) * 68;
; #pragma unroll
;             for (int i = 0; i < 4; ++i) { const f32x4 w0 = *(const LAS f32x4*)(wg + 16 * i), w1 = *(const LAS f32x4*)(wg + 16 * i + 4), w2 = *(const LAS f32x4*)(wg + 16 * i + 8), w3 = *(const LAS f32x4*)(wg + 16 * i + 12);
;                 const r_f32x2 wv[8] = {{w0[0], w0[1]}, {w0[2], w0[3]}, {w1[0], w1[1]}, {w1[2], w1[3]}, {w2[0], w2[1]}, {w2[2], w2[3]}, {w3[0], w3[1]}, {w3[2], w3[3]}};
; #pragma unroll
;                 for (int q = 0; q < 4; ++q) { const float h = xx[q][j][i]; const r_f32x2 hh = {h, h};
; #pragma unroll
;                     for (int e = 0; e < 8; ++e) lg2[q][e] = __builtin_elementwise_fma(hh, wv[e], lg2[q][e]); }
; #pragma unroll
;                 for (int q = 0; q < 4; ++q)
;                     asm volatile("" : "+v"(lg2[q][0]), "+v"(lg2[q][1]), "+v"(lg2[q][2]), "+v"(lg2[q][3]), "+v"(lg2[q][4]), "+v"(lg2[q][5]), "+v"(lg2[q][6]), "+v"(lg2[q][7]));
;                 } }
	v_pk_fma_f32 v[94:95], v[28:29], v[64:65], v[94:95] op_sel:[1,0,0]
	v_pk_fma_f32 v[28:29], v[28:29], v[66:67], v[32:33] op_sel:[1,0,0]
	v_pk_fma_f32 v[32:33], v[52:53], v[10:11], v[54:55] op_sel:[1,0,0]
	v_pk_fma_f32 v[96:97], v[52:53], v[12:13], v[96:97] op_sel:[1,0,0]
	v_pk_fma_f32 v[100:101], v[52:53], v[14:15], v[100:101] op_sel:[1,0,0]
	v_pk_fma_f32 v[102:103], v[52:53], v[16:17], v[102:103] op_sel:[1,0,0]
	v_pk_fma_f32 v[104:105], v[52:53], v[58:59], v[104:105] op_sel:[1,0,0]
	v_pk_fma_f32 v[106:107], v[52:53], v[60:61], v[106:107] op_sel:[1,0,0]
	v_pk_fma_f32 v[108:109], v[52:53], v[64:65], v[108:109] op_sel:[1,0,0]
	v_pk_fma_f32 v[70:71], v[52:53], v[66:67], v[70:71] op_sel:[1,0,0]
	v_pk_fma_f32 v[110:111], v[68:69], v[10:11], v[110:111] op_sel:[1,0,0]
	v_pk_fma_f32 v[112:113], v[68:69], v[12:13], v[112:113] op_sel:[1,0,0]
	v_pk_fma_f32 v[114:115], v[68:69], v[14:15], v[114:115] op_sel:[1,0,0]
	v_pk_fma_f32 v[116:117], v[68:69], v[16:17], v[116:117] op_sel:[1,0,0]
	v_pk_fma_f32 v[118:119], v[68:69], v[58:59], v[118:119] op_sel:[1,0,0]
	v_pk_fma_f32 v[120:121], v[68:69], v[60:61], v[120:121] op_sel:[1,0,0]
	v_pk_fma_f32 v[122:123], v[68:69], v[64:65], v[122:123] op_sel:[1,0,0]
	v_pk_fma_f32 v[68:69], v[68:69], v[66:67], v[72:73] op_sel:[1,0,0]
	v_pk_fma_f32 v[72:73], v[8:9], v[10:11], v[124:125] op_sel:[1,0,0]
	v_pk_fma_f32 v[124:125], v[8:9], v[12:13], v[126:127] op_sel:[1,0,0]
	v_pk_fma_f32 v[126:127], v[8:9], v[14:15], v[128:129] op_sel:[1,0,0]
	v_pk_fma_f32 v[16:17], v[8:9], v[16:17], v[130:131] op_sel:[1,0,0]
	v_pk_fma_f32 v[74:75], v[8:9], v[58:59], v[74:75] op_sel:[1,0,0]
	v_pk_fma_f32 v[76:77], v[8:9], v[60:61], v[76:77] op_sel:[1,0,0]
	v_pk_fma_f32 v[64:65], v[8:9], v[64:65], v[78:79] op_sel:[1,0,0]
	v_pk_fma_f32 v[66:67], v[8:9], v[66:67], v[80:81] op_sel:[1,0,0]
	s_nop 0
	ds_read_b128 v[8:11], v1 offset:34944
	ds_read_b128 v[12:15], v1 offset:34960
	ds_read_b128 v[52:55], v1 offset:34976
	ds_read_b128 v[58:61], v1 offset:34992
	s_waitcnt lgkmcnt(3)
	v_pk_fma_f32 v[78:79], v[24:25], v[8:9], v[82:83] op_sel_hi:[0,1,1]
	v_pk_fma_f32 v[80:81], v[24:25], v[10:11], v[84:85] op_sel_hi:[0,1,1]
	s_waitcnt lgkmcnt(2)
	v_pk_fma_f32 v[82:83], v[24:25], v[12:13], v[86:87] op_sel_hi:[0,1,1]
	v_pk_fma_f32 v[84:85], v[24:25], v[14:15], v[88:89] op_sel_hi:[0,1,1]
	s_waitcnt lgkmcnt(1)
	v_pk_fma_f32 v[86:87], v[24:25], v[52:53], v[90:91] op_sel_hi:[0,1,1]
	v_pk_fma_f32 v[88:89], v[24:25], v[54:55], v[92:93] op_sel_hi:[0,1,1]
	s_waitcnt lgkmcnt(0)
	v_pk_fma_f32 v[90:91], v[24:25], v[58:59], v[94:95] op_sel_hi:[0,1,1]
	v_pk_fma_f32 v[28:29], v[24:25], v[60:61], v[28:29] op_sel_hi:[0,1,1]
	v_pk_fma_f32 v[32:33], v[30:31], v[8:9], v[32:33] op_sel_hi:[0,1,1]
	v_pk_fma_f32 v[92:93], v[30:31], v[10:11], v[96:97] op_sel_hi:[0,1,1]
	v_pk_fma_f32 v[94:95], v[30:31], v[12:13], v[100:101] op_sel_hi:[0,1,1]
	v_pk_fma_f32 v[96:97], v[30:31], v[14:15], v[102:103] op_sel_hi:[0,1,1]
	v_pk_fma_f32 v[100:101], v[30:31], v[52:53], v[104:105] op_sel_hi:[0,1,1]
	v_pk_fma_f32 v[102:103], v[30:31], v[54:55], v[106:107] op_sel_hi:[0,1,1]
	v_pk_fma_f32 v[104:105], v[30:31], v[58:59], v[108:109] op_sel_hi:[0,1,1]
	v_pk_fma_f32 v[70:71], v[30:31], v[60:61], v[70:71] op_sel_hi:[0,1,1]
	v_pk_fma_f32 v[106:107], v[62:63], v[8:9], v[110:111] op_sel_hi:[0,1,1]
	v_pk_fma_f32 v[108:109], v[62:63], v[10:11], v[112:113] op_sel_hi:[0,1,1]
	v_pk_fma_f32 v[110:111], v[62:63], v[12:13], v[114:115] op_sel_hi:[0,1,1]
	v_pk_fma_f32 v[112:113], v[62:63], v[14:15], v[116:117] op_sel_hi:[0,1,1]
	v_pk_fma_f32 v[114:115], v[62:63], v[52:53], v[118:119] op_sel_hi:[0,1,1]
	v_pk_fma_f32 v[116:117], v[62:63], v[54:55], v[120:121] op_sel_hi:[0,1,1]
	v_pk_fma_f32 v[118:119], v[62:63], v[58:59], v[122:123] op_sel_hi:[0,1,1]
	v_pk_fma_f32 v[68:69], v[62:63], v[60:61], v[68:69] op_sel_hi:[0,1,1]
	v_pk_fma_f32 v[72:73], v[6:7], v[8:9], v[72:73] op_sel_hi:[0,1,1]
	v_pk_fma_f32 v[120:121], v[6:7], v[10:11], v[124:125] op_sel_hi:[0,1,1]
	v_pk_fma_f32 v[122:123], v[6:7], v[12:13], v[126:127] op_sel_hi:[0,1,1]
	v_pk_fma_f32 v[16:17], v[6:7], v[14:15], v[16:17] op_sel_hi:[0,1,1]
	v_pk_fma_f32 v[74:75], v[6:7], v[52:53], v[74:75] op_sel_hi:[0,1,1]
	v_pk_fma_f32 v[76:77], v[6:7], v[54:55], v[76:77] op_sel_hi:[0,1,1]
	v_pk_fma_f32 v[64:65], v[6:7], v[58:59], v[64:65] op_sel_hi:[0,1,1]
	v_pk_fma_f32 v[66:67], v[6:7], v[60:61], v[66:67] op_sel_hi:[0,1,1]
	ds_read_b128 v[8:11], v1 offset:35008
	ds_read_b128 v[12:15], v1 offset:35024
	ds_read_b128 v[52:55], v1 offset:35040
	ds_read_b128 v[58:61], v1 offset:35056
	s_waitcnt lgkmcnt(3)
	v_pk_fma_f32 v[78:79], v[24:25], v[8:9], v[78:79] op_sel:[1,0,0]
	v_pk_fma_f32 v[80:81], v[24:25], v[10:11], v[80:81] op_sel:[1,0,0]
	s_waitcnt lgkmcnt(2)
	v_pk_fma_f32 v[82:83], v[24:25], v[12:13], v[82:83] op_sel:[1,0,0]
	v_pk_fma_f32 v[84:85], v[24:25], v[14:15], v[84:85] op_sel:[1,0,0]
	s_waitcnt lgkmcnt(1)
	v_pk_fma_f32 v[86:87], v[24:25], v[52:53], v[86:87] op_sel:[1,0,0]
	v_pk_fma_f32 v[88:89], v[24:25], v[54:55], v[88:89] op_sel:[1,0,0]
	s_waitcnt lgkmcnt(0)
; #define LAS __attribute__((address_space(3)))
; __device__ __forceinline__ void phase_post_mix(Frame& F, int l) {
;     ...
;         for (int j = 0; j < 4; ++j) { const LAS float* wg = rws + (lane + 64 * j) * 68;
; #pragma unroll
;             for (int i = 0; i < 4; ++i) { const f32x4 w0 = *(const LAS f32x4*)(wg + 16 * i), w1 = *(const LAS f32x4*)(wg + 16 * i + 4), w2 = *(const LAS f32x4*)(wg + 16 * i + 8), w3 = *(const LAS f32x4*)(wg + 16 * i + 12);
;                 const r_f32x2 wv[8] = {{w0[0], w0[1]}, {w0[2], w0[3]}, {w1[0], w1[1]}, {w1[2], w1[3]}, {w2[0], w2[1]}, {w2[2], w2[3]}, {w3[0], w3[1]}, {w3[2], w3[3]}};
; #pragma unroll
;                 for (int q = 0; q < 4; ++q) { const float h = xx[q][j][i]; const r_f32x2 hh = {h, h};
; #pragma unroll
;                     for (int e = 0; e < 8; ++e) lg2[q][e] = __builtin_elementwise_fma(hh, wv[e], lg2[q][e]); }
; #pragma unroll
;                 for (int q = 0; q < 4; ++q)
;                     asm volatile("" : "+v"(lg2[q][0]), "+v"(lg2[q][1]), "+v"(lg2[q][2]), "+v"(lg2[q][3]), "+v"(lg2[q][4]), "+v"(lg2[q][5]), "+v"(lg2[q][6]), "+v"(lg2[q][7]));
;                 } }
	v_pk_fma_f32 v[90:91], v[24:25], v[58:59], v[90:91] op_sel:[1,0,0]
	v_pk_fma_f32 v[24:25], v[24:25], v[60:61], v[28:29] op_sel:[1,0,0]
	v_pk_fma_f32 v[32:33], v[30:31], v[8:9], v[32:33] op_sel:[1,0,0]
	v_pk_fma_f32 v[92:93], v[30:31], v[10:11], v[92:93] op_sel:[1,0,0]
	v_pk_fma_f32 v[94:95], v[30:31], v[12:13], v[94:95] op_sel:[1,0,0]
	v_pk_fma_f32 v[96:97], v[30:31], v[14:15], v[96:97] op_sel:[1,0,0]
	v_pk_fma_f32 v[100:101], v[30:31], v[52:53], v[100:101] op_sel:[1,0,0]
	v_pk_fma_f32 v[102:103], v[30:31], v[54:55], v[102:103] op_sel:[1,0,0]
	v_pk_fma_f32 v[104:105], v[30:31], v[58:59], v[104:105] op_sel:[1,0,0]
	v_pk_fma_f32 v[70:71], v[30:31], v[60:61], v[70:71] op_sel:[1,0,0]
	v_pk_fma_f32 v[106:107], v[62:63], v[8:9], v[106:107] op_sel:[1,0,0]
	v_pk_fma_f32 v[108:109], v[62:63], v[10:11], v[108:109] op_sel:[1,0,0]
	v_pk_fma_f32 v[110:111], v[62:63], v[12:13], v[110:111] op_sel:[1,0,0]
	v_pk_fma_f32 v[112:113], v[62:63], v[14:15], v[112:113] op_sel:[1,0,0]
	v_pk_fma_f32 v[114:115], v[62:63], v[52:53], v[114:115] op_sel:[1,0,0]
	v_pk_fma_f32 v[116:117], v[62:63], v[54:55], v[116:117] op_sel:[1,0,0]
	v_pk_fma_f32 v[118:119], v[62:63], v[58:59], v[118:119] op_sel:[1,0,0]
	v_pk_fma_f32 v[62:63], v[62:63], v[60:61], v[68:69] op_sel:[1,0,0]
	v_pk_fma_f32 v[68:69], v[6:7], v[8:9], v[72:73] op_sel:[1,0,0]
	v_pk_fma_f32 v[72:73], v[6:7], v[10:11], v[120:121] op_sel:[1,0,0]
	v_pk_fma_f32 v[120:121], v[6:7], v[12:13], v[122:123] op_sel:[1,0,0]
	v_pk_fma_f32 v[122:123], v[6:7], v[14:15], v[16:17] op_sel:[1,0,0]
	v_pk_fma_f32 v[52:53], v[6:7], v[52:53], v[74:75] op_sel:[1,0,0]
	v_pk_fma_f32 v[54:55], v[6:7], v[54:55], v[76:77] op_sel:[1,0,0]
	v_pk_fma_f32 v[58:59], v[6:7], v[58:59], v[64:65] op_sel:[1,0,0]
	v_pk_fma_f32 v[60:61], v[6:7], v[60:61], v[66:67] op_sel:[1,0,0]
	s_nop 0
	ds_read_b128 v[6:9], v1 offset:52224
	ds_read_b128 v[10:13], v1 offset:52240
	ds_read_b128 v[14:17], v1 offset:52256
	ds_read_b128 v[28:31], v1 offset:52272
	s_waitcnt lgkmcnt(3)
	v_pk_fma_f32 v[64:65], v[20:21], v[6:7], v[78:79] op_sel_hi:[0,1,1]
	v_pk_fma_f32 v[66:67], v[20:21], v[8:9], v[80:81] op_sel_hi:[0,1,1]
	s_waitcnt lgkmcnt(2)
	v_pk_fma_f32 v[74:75], v[20:21], v[10:11], v[82:83] op_sel_hi:[0,1,1]
	v_pk_fma_f32 v[76:77], v[20:21], v[12:13], v[84:85] op_sel_hi:[0,1,1]
	s_waitcnt lgkmcnt(1)
	v_pk_fma_f32 v[78:79], v[20:21], v[14:15], v[86:87] op_sel_hi:[0,1,1]
	v_pk_fma_f32 v[80:81], v[20:21], v[16:17], v[88:89] op_sel_hi:[0,1,1]
	s_waitcnt lgkmcnt(0)
	v_pk_fma_f32 v[82:83], v[20:21], v[28:29], v[90:91] op_sel_hi:[0,1,1]
	v_pk_fma_f32 v[24:25], v[20:21], v[30:31], v[24:25] op_sel_hi:[0,1,1]
	v_pk_fma_f32 v[32:33], v[26:27], v[6:7], v[32:33] op_sel_hi:[0,1,1]
	v_pk_fma_f32 v[84:85], v[26:27], v[8:9], v[92:93] op_sel_hi:[0,1,1]
	v_pk_fma_f32 v[86:87], v[26:27], v[10:11], v[94:95] op_sel_hi:[0,1,1]
	v_pk_fma_f32 v[88:89], v[26:27], v[12:13], v[96:97] op_sel_hi:[0,1,1]
	v_pk_fma_f32 v[90:91], v[26:27], v[14:15], v[100:101] op_sel_hi:[0,1,1]
	v_pk_fma_f32 v[92:93], v[26:27], v[16:17], v[102:103] op_sel_hi:[0,1,1]
	v_pk_fma_f32 v[94:95], v[26:27], v[28:29], v[104:105] op_sel_hi:[0,1,1]
	v_pk_fma_f32 v[70:71], v[26:27], v[30:31], v[70:71] op_sel_hi:[0,1,1]
	v_pk_fma_f32 v[96:97], v[56:57], v[6:7], v[106:107] op_sel_hi:[0,1,1]
	v_pk_fma_f32 v[100:101], v[56:57], v[8:9], v[108:109] op_sel_hi:[0,1,1]
	v_pk_fma_f32 v[102:103], v[56:57], v[10:11], v[110:111] op_sel_hi:[0,1,1]
	v_pk_fma_f32 v[104:105], v[56:57], v[12:13], v[112:113] op_sel_hi:[0,1,1]
	v_pk_fma_f32 v[106:107], v[56:57], v[14:15], v[114:115] op_sel_hi:[0,1,1]
	v_pk_fma_f32 v[108:109], v[56:57], v[16:17], v[116:117] op_sel_hi:[0,1,1]
	v_pk_fma_f32 v[110:111], v[56:57], v[28:29], v[118:119] op_sel_hi:[0,1,1]
	v_pk_fma_f32 v[62:63], v[56:57], v[30:31], v[62:63] op_sel_hi:[0,1,1]
	v_pk_fma_f32 v[68:69], v[4:5], v[6:7], v[68:69] op_sel_hi:[0,1,1]
	v_pk_fma_f32 v[72:73], v[4:5], v[8:9], v[72:73] op_sel_hi:[0,1,1]
	v_pk_fma_f32 v[112:113], v[4:5], v[10:11], v[120:121] op_sel_hi:[0,1,1]
	v_pk_fma_f32 v[114:115], v[4:5], v[12:13], v[122:123] op_sel_hi:[0,1,1]
	v_pk_fma_f32 v[52:53], v[4:5], v[14:15], v[52:53] op_sel_hi:[0,1,1]
	v_pk_fma_f32 v[54:55], v[4:5], v[16:17], v[54:55] op_sel_hi:[0,1,1]
	v_pk_fma_f32 v[58:59], v[4:5], v[28:29], v[58:59] op_sel_hi:[0,1,1]
	v_pk_fma_f32 v[60:61], v[4:5], v[30:31], v[60:61] op_sel_hi:[0,1,1]
	ds_read_b128 v[6:9], v1 offset:52288
	ds_read_b128 v[10:13], v1 offset:52304
	ds_read_b128 v[14:17], v1 offset:52320
	ds_read_b128 v[28:31], v1 offset:52336
	s_waitcnt lgkmcnt(3)
	v_pk_fma_f32 v[64:65], v[20:21], v[6:7], v[64:65] op_sel:[1,0,0]
	v_pk_fma_f32 v[66:67], v[20:21], v[8:9], v[66:67] op_sel:[1,0,0]
	s_waitcnt lgkmcnt(2)
	v_pk_fma_f32 v[74:75], v[20:21], v[10:11], v[74:75] op_sel:[1,0,0]
	v_pk_fma_f32 v[76:77], v[20:21], v[12:13], v[76:77] op_sel:[1,0,0]
	s_waitcnt lgkmcnt(1)
	v_pk_fma_f32 v[78:79], v[20:21], v[14:15], v[78:79] op_sel:[1,0,0]
	v_pk_fma_f32 v[80:81], v[20:21], v[16:17], v[80:81] op_sel:[1,0,0]
	s_waitcnt lgkmcnt(0)
; #define LAS __attribute__((address_space(3)))
; __device__ __forceinline__ void phase_post_mix(Frame& F, int l) {
;     ...
;         for (int j = 0; j < 4; ++j) { const LAS float* wg = rws + (lane + 64 * j) * 68;
; #pragma unroll
;             for (int i = 0; i < 4; ++i) { const f32x4 w0 = *(const LAS f32x4*)(wg + 16 * i), w1 = *(const LAS f32x4*)(wg + 16 * i + 4), w2 = *(const LAS f32x4*)(wg + 16 * i + 8), w3 = *(const LAS f32x4*)(wg + 16 * i + 12);
;                 const r_f32x2 wv[8] = {{w0[0], w0[1]}, {w0[2], w0[3]}, {w1[0], w1[1]}, {w1[2], w1[3]}, {w2[0], w2[1]}, {w2[2], w2[3]}, {w3[0], w3[1]}, {w3[2], w3[3]}};
; #pragma unroll
;                 for (int q = 0; q < 4; ++q) { const float h = xx[q][j][i]; const r_f32x2 hh = {h, h};
; #pragma unroll
;                     for (int e = 0; e < 8; ++e) lg2[q][e] = __builtin_elementwise_fma(hh, wv[e], lg2[q][e]); }
; #pragma unroll
;                 for (int q = 0; q < 4; ++q)
;                     asm volatile("" : "+v"(lg2[q][0]), "+v"(lg2[q][1]), "+v"(lg2[q][2]), "+v"(lg2[q][3]), "+v"(lg2[q][4]), "+v"(lg2[q][5]), "+v"(lg2[q][6]), "+v"(lg2[q][7]));
;                 } }
	v_pk_fma_f32 v[82:83], v[20:21], v[28:29], v[82:83] op_sel:[1,0,0]
	v_pk_fma_f32 v[20:21], v[20:21], v[30:31], v[24:25] op_sel:[1,0,0]
	v_pk_fma_f32 v[32:33], v[26:27], v[6:7], v[32:33] op_sel:[1,0,0]
	v_pk_fma_f32 v[84:85], v[26:27], v[8:9], v[84:85] op_sel:[1,0,0]
	v_pk_fma_f32 v[86:87], v[26:27], v[10:11], v[86:87] op_sel:[1,0,0]
	v_pk_fma_f32 v[88:89], v[26:27], v[12:13], v[88:89] op_sel:[1,0,0]
	v_pk_fma_f32 v[90:91], v[26:27], v[14:15], v[90:91] op_sel:[1,0,0]
	v_pk_fma_f32 v[92:93], v[26:27], v[16:17], v[92:93] op_sel:[1,0,0]
	v_pk_fma_f32 v[94:95], v[26:27], v[28:29], v[94:95] op_sel:[1,0,0]
	v_pk_fma_f32 v[70:71], v[26:27], v[30:31], v[70:71] op_sel:[1,0,0]
	v_pk_fma_f32 v[96:97], v[56:57], v[6:7], v[96:97] op_sel:[1,0,0]
	v_pk_fma_f32 v[100:101], v[56:57], v[8:9], v[100:101] op_sel:[1,0,0]
	v_pk_fma_f32 v[102:103], v[56:57], v[10:11], v[102:103] op_sel:[1,0,0]
	v_pk_fma_f32 v[104:105], v[56:57], v[12:13], v[104:105] op_sel:[1,0,0]
	v_pk_fma_f32 v[106:107], v[56:57], v[14:15], v[106:107] op_sel:[1,0,0]
	v_pk_fma_f32 v[108:109], v[56:57], v[16:17], v[108:109] op_sel:[1,0,0]
	v_pk_fma_f32 v[110:111], v[56:57], v[28:29], v[110:111] op_sel:[1,0,0]
	v_pk_fma_f32 v[56:57], v[56:57], v[30:31], v[62:63] op_sel:[1,0,0]
	v_pk_fma_f32 v[62:63], v[4:5], v[6:7], v[68:69] op_sel:[1,0,0]
	v_pk_fma_f32 v[68:69], v[4:5], v[8:9], v[72:73] op_sel:[1,0,0]
	v_pk_fma_f32 v[72:73], v[4:5], v[10:11], v[112:113] op_sel:[1,0,0]
	v_pk_fma_f32 v[112:113], v[4:5], v[12:13], v[114:115] op_sel:[1,0,0]
	v_pk_fma_f32 v[52:53], v[4:5], v[14:15], v[52:53] op_sel:[1,0,0]
	v_pk_fma_f32 v[16:17], v[4:5], v[16:17], v[54:55] op_sel:[1,0,0]
	v_pk_fma_f32 v[28:29], v[4:5], v[28:29], v[58:59] op_sel:[1,0,0]
	v_pk_fma_f32 v[30:31], v[4:5], v[30:31], v[60:61] op_sel:[1,0,0]
	s_nop 0
	ds_read_b128 v[4:7], v1 offset:52352
	ds_read_b128 v[8:11], v1 offset:52368
	ds_read_b128 v[12:15], v1 offset:52384
	ds_read_b128 v[24:27], v1 offset:52400
	s_waitcnt lgkmcnt(3)
	v_pk_fma_f32 v[54:55], v[18:19], v[4:5], v[64:65] op_sel_hi:[0,1,1]
	v_pk_fma_f32 v[58:59], v[18:19], v[6:7], v[66:67] op_sel_hi:[0,1,1]
	s_waitcnt lgkmcnt(2)
	v_pk_fma_f32 v[60:61], v[18:19], v[8:9], v[74:75] op_sel_hi:[0,1,1]
	v_pk_fma_f32 v[64:65], v[18:19], v[10:11], v[76:77] op_sel_hi:[0,1,1]
	s_waitcnt lgkmcnt(1)
	v_pk_fma_f32 v[66:67], v[18:19], v[12:13], v[78:79] op_sel_hi:[0,1,1]
	v_pk_fma_f32 v[80:81], v[18:19], v[14:15], v[80:81] op_sel_hi:[0,1,1]
	s_waitcnt lgkmcnt(0)
	v_pk_fma_f32 v[82:83], v[18:19], v[24:25], v[82:83] op_sel_hi:[0,1,1]
	v_pk_fma_f32 v[20:21], v[18:19], v[26:27], v[20:21] op_sel_hi:[0,1,1]
	v_pk_fma_f32 v[32:33], v[22:23], v[4:5], v[32:33] op_sel_hi:[0,1,1]
	v_pk_fma_f32 v[84:85], v[22:23], v[6:7], v[84:85] op_sel_hi:[0,1,1]
	v_pk_fma_f32 v[86:87], v[22:23], v[8:9], v[86:87] op_sel_hi:[0,1,1]
	v_pk_fma_f32 v[88:89], v[22:23], v[10:11], v[88:89] op_sel_hi:[0,1,1]
	v_pk_fma_f32 v[90:91], v[22:23], v[12:13], v[90:91] op_sel_hi:[0,1,1]
	v_pk_fma_f32 v[92:93], v[22:23], v[14:15], v[92:93] op_sel_hi:[0,1,1]
	v_pk_fma_f32 v[94:95], v[22:23], v[24:25], v[94:95] op_sel_hi:[0,1,1]
	v_pk_fma_f32 v[114:115], v[22:23], v[26:27], v[70:71] op_sel_hi:[0,1,1]
	v_pk_fma_f32 v[96:97], v[50:51], v[4:5], v[96:97] op_sel_hi:[0,1,1]
	v_pk_fma_f32 v[100:101], v[50:51], v[6:7], v[100:101] op_sel_hi:[0,1,1]
	v_pk_fma_f32 v[102:103], v[50:51], v[8:9], v[102:103] op_sel_hi:[0,1,1]
	v_pk_fma_f32 v[104:105], v[50:51], v[10:11], v[104:105] op_sel_hi:[0,1,1]
	v_pk_fma_f32 v[106:107], v[50:51], v[12:13], v[106:107] op_sel_hi:[0,1,1]
	v_pk_fma_f32 v[108:109], v[50:51], v[14:15], v[108:109] op_sel_hi:[0,1,1]
	v_pk_fma_f32 v[110:111], v[50:51], v[24:25], v[110:111] op_sel_hi:[0,1,1]
	v_pk_fma_f32 v[116:117], v[50:51], v[26:27], v[56:57] op_sel_hi:[0,1,1]
	v_pk_fma_f32 v[118:119], v[2:3], v[4:5], v[62:63] op_sel_hi:[0,1,1]
	v_pk_fma_f32 v[120:121], v[2:3], v[6:7], v[68:69] op_sel_hi:[0,1,1]
	v_pk_fma_f32 v[8:9], v[2:3], v[8:9], v[72:73] op_sel_hi:[0,1,1]
	v_pk_fma_f32 v[112:113], v[2:3], v[10:11], v[112:113] op_sel_hi:[0,1,1]
	v_pk_fma_f32 v[12:13], v[2:3], v[12:13], v[52:53] op_sel_hi:[0,1,1]
	v_pk_fma_f32 v[122:123], v[2:3], v[14:15], v[16:17] op_sel_hi:[0,1,1]
	v_pk_fma_f32 v[124:125], v[2:3], v[24:25], v[28:29] op_sel_hi:[0,1,1]
	v_pk_fma_f32 v[126:127], v[2:3], v[26:27], v[30:31] op_sel_hi:[0,1,1]
	ds_read_b128 v[4:7], v1 offset:52416
	ds_read_b128 v[68:71], v1 offset:52432
	ds_read_b128 v[72:75], v1 offset:52448
	ds_read_b128 v[76:79], v1 offset:52464
	s_waitcnt lgkmcnt(3)
	v_pk_fma_f32 v[128:129], v[18:19], v[4:5], v[54:55] op_sel:[1,0,0]
	v_pk_fma_f32 v[130:131], v[18:19], v[6:7], v[58:59] op_sel:[1,0,0]
	s_waitcnt lgkmcnt(2)
	v_pk_fma_f32 v[132:133], v[18:19], v[68:69], v[60:61] op_sel:[1,0,0]
	v_pk_fma_f32 v[134:135], v[18:19], v[70:71], v[64:65] op_sel:[1,0,0]
	s_waitcnt lgkmcnt(1)
	v_pk_fma_f32 v[136:137], v[18:19], v[72:73], v[66:67] op_sel:[1,0,0]
	v_pk_fma_f32 v[80:81], v[18:19], v[74:75], v[80:81] op_sel:[1,0,0]
	s_waitcnt lgkmcnt(0)
; #define LAS __attribute__((address_space(3)))
; __device__ __forceinline__ void post_mix_route(Frame& F, int m, float (&lg)[16]) {
;     const int lane = F.lane, b = m >> 12, t = m & (SEQ - 1);
;     const bool b5 = (lane & 32) != 0, b4 = (lane & 16) != 0, b3 = (lane & 8) != 0, b2 = (lane & 4) != 0;
;     float a8[8], a4[4], a2[2];
; #pragma unroll
;     for (int e = 0; e < 8; ++e) a8[e] = swap32_sum(lg[e], lg[8 + e]);
; #pragma unroll
;     for (int e = 0; e < 4; ++e) a4[e] = swap16_sum(a8[e], a8[4 + e]);
; #pragma unroll
;     for (int e = 0; e < 2; ++e) { const float keep = b3 ? a4[2 + e] : a4[e], send = b3 ? a4[e] : a4[2 + e]; a2[e] = keep + dpp_f<DPP_ROR8>(send); }
;     float v = (b2 ? a2[1] : a2[0]) + dpp_f<DPP_HMIR>(b2 ? a2[0] : a2[1]);
;     v += dpp_f<DPP_X2>(v); v += dpp_f<DPP_X1>(v);
;     float mx = fmaxf(v, dpp_f<DPP_HMIR>(v)); mx = fmaxf(mx, dpp_f<DPP_ROR8>(mx)); mx = swap16_max(mx); mx = swap32_max(mx);
; __device__ __forceinline__ void phase_post_mix(Frame& F, int l) {
;     ...
;         for (int j = 0; j < 4; ++j) { const LAS float* wg = rws + (lane + 64 * j) * 68;
; #pragma unroll
;             for (int i = 0; i < 4; ++i) { const f32x4 w0 = *(const LAS f32x4*)(wg + 16 * i), w1 = *(const LAS f32x4*)(wg + 16 * i + 4), w2 = *(const LAS f32x4*)(wg + 16 * i + 8), w3 = *(const LAS f32x4*)(wg + 16 * i + 12);
;                 const r_f32x2 wv[8] = {{w0[0], w0[1]}, {w0[2], w0[3]}, {w1[0], w1[1]}, {w1[2], w1[3]}, {w2[0], w2[1]}, {w2[2], w2[3]}, {w3[0], w3[1]}, {w3[2], w3[3]}};
; #pragma unroll
;                 for (int q = 0; q < 4; ++q) { const float h = xx[q][j][i]; const r_f32x2 hh = {h, h};
; #pragma unroll
;                     for (int e = 0; e < 8; ++e) lg2[q][e] = __builtin_elementwise_fma(hh, wv[e], lg2[q][e]); }
; #pragma unroll
;                 for (int q = 0; q < 4; ++q)
;                     asm volatile("" : "+v"(lg2[q][0]), "+v"(lg2[q][1]), "+v"(lg2[q][2]), "+v"(lg2[q][3]), "+v"(lg2[q][4]), "+v"(lg2[q][5]), "+v"(lg2[q][6]), "+v"(lg2[q][7]));
;                 } }
;         float lg[4][16];
; #pragma unroll
;         for (int q = 0; q < 4; ++q)
; #pragma unroll
;             for (int e = 0; e < 8; ++e) { lg[q][2 * e] = lg2[q][e].x; lg[q][2 * e + 1] = lg2[q][e].y; }
; #pragma unroll
;         for (int q = 0; q < 4; ++q) if (q == 0 || mm[q] != m0) post_mix_route(F, mm[q], lg[q]);
	v_pk_fma_f32 v[82:83], v[18:19], v[76:77], v[82:83] op_sel:[1,0,0]
	v_pk_fma_f32 v[138:139], v[18:19], v[78:79], v[20:21] op_sel:[1,0,0]
	v_pk_fma_f32 v[64:65], v[22:23], v[4:5], v[32:33] op_sel:[1,0,0]
	v_pk_fma_f32 v[60:61], v[22:23], v[6:7], v[84:85] op_sel:[1,0,0]
	v_permlane32_swap_b32_e32 v128, v136
	v_permlane32_swap_b32_e32 v129, v137
	v_permlane32_swap_b32_e32 v130, v80
	v_permlane32_swap_b32_e32 v131, v81
	v_permlane32_swap_b32_e32 v132, v82
	v_permlane32_swap_b32_e32 v133, v83
	v_permlane32_swap_b32_e32 v134, v138
	v_permlane32_swap_b32_e32 v135, v139
	v_pk_fma_f32 v[56:57], v[22:23], v[68:69], v[86:87] op_sel:[1,0,0]
	v_pk_fma_f32 v[52:53], v[22:23], v[70:71], v[88:89] op_sel:[1,0,0]
	v_pk_fma_f32 v[66:67], v[22:23], v[72:73], v[90:91] op_sel:[1,0,0]
	v_pk_fma_f32 v[62:63], v[22:23], v[74:75], v[92:93] op_sel:[1,0,0]
	v_pk_fma_f32 v[58:59], v[22:23], v[76:77], v[94:95] op_sel:[1,0,0]
	v_pk_fma_f32 v[54:55], v[22:23], v[78:79], v[114:115] op_sel:[1,0,0]
	v_pk_fma_f32 v[30:31], v[50:51], v[4:5], v[96:97] op_sel:[1,0,0]
	v_pk_fma_f32 v[26:27], v[50:51], v[6:7], v[100:101] op_sel:[1,0,0]
	v_pk_fma_f32 v[22:23], v[50:51], v[68:69], v[102:103] op_sel:[1,0,0]
	v_pk_fma_f32 v[18:19], v[50:51], v[70:71], v[104:105] op_sel:[1,0,0]
	v_pk_fma_f32 v[32:33], v[50:51], v[72:73], v[106:107] op_sel:[1,0,0]
	v_pk_fma_f32 v[28:29], v[50:51], v[74:75], v[108:109] op_sel:[1,0,0]
	v_pk_fma_f32 v[24:25], v[50:51], v[76:77], v[110:111] op_sel:[1,0,0]
	v_pk_fma_f32 v[20:21], v[50:51], v[78:79], v[116:117] op_sel:[1,0,0]
	v_pk_fma_f32 v[14:15], v[2:3], v[4:5], v[118:119] op_sel:[1,0,0]
	v_pk_fma_f32 v[10:11], v[2:3], v[6:7], v[120:121] op_sel:[1,0,0]
	v_pk_fma_f32 v[6:7], v[2:3], v[68:69], v[8:9] op_sel:[1,0,0]
	v_pk_fma_f32 v[4:5], v[2:3], v[70:71], v[112:113] op_sel:[1,0,0]
	v_pk_fma_f32 v[16:17], v[2:3], v[72:73], v[12:13] op_sel:[1,0,0]
	v_add_f32_e32 v50, v128, v136
	v_add_f32_e32 v51, v129, v137
	v_add_f32_e32 v68, v130, v80
	v_add_f32_e32 v69, v131, v81
	v_add_f32_e32 v70, v132, v82
	v_add_f32_e32 v71, v133, v83
	v_add_f32_e32 v72, v134, v138
	v_add_f32_e32 v73, v135, v139
	v_permlane16_swap_b32_e32 v50, v70
	v_permlane16_swap_b32_e32 v51, v71
	v_permlane16_swap_b32_e32 v68, v72
	v_permlane16_swap_b32_e32 v69, v73
	v_add_f32_e32 v50, v50, v70
	v_add_f32_e32 v51, v51, v71
	v_add_f32_e32 v68, v68, v72
	v_add_f32_e32 v69, v69, v73
	v_cndmask_b32_e64 v70, v68, v50, s[4:5]
	v_cndmask_b32_e64 v50, v50, v68, s[4:5]
	v_cndmask_b32_e64 v68, v69, v51, s[4:5]
	v_cndmask_b32_e64 v51, v51, v69, s[4:5]
	v_add_f32_dpp v50, v50, v70 row_ror:8 row_mask:0xf bank_mask:0xf bound_ctrl:1
	v_pk_fma_f32 v[12:13], v[2:3], v[74:75], v[122:123] op_sel:[1,0,0]
	v_add_f32_dpp v51, v51, v68 row_ror:8 row_mask:0xf bank_mask:0xf bound_ctrl:1
	v_cndmask_b32_e64 v68, v51, v50, s[6:7]
	v_cndmask_b32_e64 v50, v50, v51, s[6:7]
	v_pk_fma_f32 v[8:9], v[2:3], v[76:77], v[124:125] op_sel:[1,0,0]
	v_pk_fma_f32 v[2:3], v[2:3], v[78:79], v[126:127] op_sel:[1,0,0]
	v_add_f32_dpp v50, v50, v68 row_half_mirror row_mask:0xf bank_mask:0xf bound_ctrl:1
	s_nop 1
	v_add_f32_dpp v50, v50, v50 quad_perm:[2,3,0,1] row_mask:0xf bank_mask:0xf bound_ctrl:1
	s_nop 1
	v_add_f32_dpp v50, v50, v50 quad_perm:[1,0,3,2] row_mask:0xf bank_mask:0xf bound_ctrl:1
	s_nop 1
	v_mov_b32_dpp v51, v50 row_half_mirror row_mask:0xf bank_mask:0xf bound_ctrl:1
	v_max_f32_e32 v51, v51, v51
	v_max_f32_e32 v51, v50, v51
	s_nop 1
	v_mov_b32_dpp v68, v51 row_ror:8 row_mask:0xf bank_mask:0xf bound_ctrl:1
	v_max_f32_e32 v68, v68, v68
	v_max_f32_e32 v51, v51, v68
	v_mov_b32_e32 v68, v51
	s_nop 1
	v_permlane16_swap_b32_e32 v51, v68
	v_max_f32_e32 v68, v68, v68
	v_max_f32_e32 v51, v51, v51
	v_max_f32_e32 v51, v51, v68
	v_mov_b32_e32 v68, v51
	s_nop 1
	v_permlane32_swap_b32_e32 v51, v68
	v_max_f32_e32 v68, v68, v68
	v_max_f32_e32 v51, v51, v51
	v_max_f32_e32 v51, v51, v68
	v_sub_f32_e32 v50, v50, v51
	v_mul_f32_e32 v51, 0x3fb8aa3b, v50
	v_fma_f32 v68, v50, s78, -v51
	v_rndne_f32_e32 v69, v51
	v_fmac_f32_e32 v68, 0x32a5705f, v50
	v_sub_f32_e32 v51, v51, v69
	v_add_f32_e32 v51, v51, v68
	v_exp_f32_e32 v51, v51
	v_cvt_i32_f32_e32 v68, v69
	v_cmp_ngt_f32_e32 vcc, s2, v50
	s_mov_b32 s2, 0x42b17218
	v_ldexp_f32 v51, v51, v68
	v_cndmask_b32_e32 v51, 0, v51, vcc
	v_cmp_nlt_f32_e32 vcc, s2, v50
	s_nop 1
	v_cndmask_b32_e32 v50, v242, v51, vcc
	s_nop 1
	v_add_f32_dpp v51, v50, v50 row_half_mirror row_mask:0xf bank_mask:0xf bound_ctrl:1
	s_nop 1
	v_add_f32_dpp v51, v51, v51 row_ror:8 row_mask:0xf bank_mask:0xf bound_ctrl:1
	v_mov_b32_e32 v68, v51
	s_nop 1
	v_permlane16_swap_b32_e32 v51, v68
	v_add_f32_e32 v51, v51, v68
	v_mov_b32_e32 v68, v51
	s_nop 1
	v_permlane32_swap_b32_e32 v51, v68
	s_and_saveexec_b64 s[2:3], s[8:9]
	s_cbranch_execnz .LBB0_1253
	s_or_b64 exec, exec, s[2:3]
	s_cmp_eq_u32 s14, s28
	s_cbranch_scc0 .LBB0_1254
